# hand-scheduled scan phase (RG-LRU carry-in + 64-row scan with gelu): rolling 8-deep load prefetch instead of the compiler's load-wait-per-row; same arithmetic
# speedup vs baseline: 1.0117x; 1.0117x over previous
; #define RP(n) _Pragma("nounroll") for (int rep_ = 0; rep_ < (int)(((REPEAT) >> (n)) & 1u) + 1; ++rep_)
; #define IDS() const int tid = opaque_tid(), lane = tid & 63, gtid = bx * NTHREADS + tid; (void)lane; (void)gtid
; __global__ void __launch_bounds__(NTHREADS, 2) fwd_kernel(Args args) {
;     ...
;     if (PH(5)) RP(5)
;     {
;         IDS();
;         const unsigned* __restrict__ AB = (const unsigned*)(ws + A_AV);
;         const float* __restrict__ AGA = (const float*)(ws + WS_AGGA); const float* __restrict__ AGB = (const float*)(ws + WS_AGGB);
;         const bf16_t* __restrict__ U = (const bf16_t*)(ws + A_U); bf16_t* __restrict__ Y = (bf16_t*)(ws + A_Y);
;         for (int item = bx; item < NBATCH * NCH; item += G) {
;             const int b = item / NCH, ch = item - b * NCH; const size_t r0 = (size_t)item * SCH;
;             f32x4 h = {0.f, 0.f, 0.f, 0.f};
; #pragma unroll 8
;             for (int c = 0; c < ch; ++c) { const f32x4 a = *(const f32x4*)(AGA + (size_t)(b * NCH + c) * D + 4 * tid), bb = *(const f32x4*)(AGB + (size_t)(b * NCH + c) * D + 4 * tid); h = a * h + bb; }
; #pragma unroll 8
;             for (int t = 0; t < SCH; ++t) {
;                 const u32x4 pw = *(const u32x4*)(AB + (r0 + t) * D + 4 * tid);
.LBB0_390:
	s_or_b64 exec, exec, s[4:5]
	s_waitcnt lgkmcnt(0)
	v_mov_b32_e32 v2, v0
	s_and_b64 vcc, exec, s[22:23]
	s_barrier
	s_cbranch_vccz .LBB0_404
	v_lshlrev_b32_e32 v4, 4, v2
	v_lshlrev_b32_e32 v5, 3, v2
	s_mov_b32 s62, s2
.Lp5_item:
	s_lshr_b32 s0, s62, 6
	s_and_b32 s1, s62, 63
	s_lshl_b32 s4, s62, 19
	s_lshl_b32 s5, s62, 18
	s_add_u32 s42, s70, 0x42a00000
	s_addc_u32 s43, s71, 0
	s_add_u32 s42, s42, s4
	s_addc_u32 s43, s43, 0
	s_add_u32 s44, s70, 0x36a00000
	s_addc_u32 s45, s71, 0
	s_add_u32 s44, s44, s4
	s_addc_u32 s45, s45, 0
	s_add_u32 s46, s70, 0x52a00000
	s_addc_u32 s47, s71, 0
	s_add_u32 s46, s46, s5
	s_addc_u32 s47, s47, 0
	global_load_dwordx4 v[10:13], v4, s[42:43]
	global_load_dwordx2 v[14:15], v5, s[44:45]
	s_add_u32 s42, s42, 0x2000
	s_addc_u32 s43, s43, 0
	s_add_u32 s44, s44, 0x2000
	s_addc_u32 s45, s45, 0
	global_load_dwordx4 v[16:19], v4, s[42:43]
	global_load_dwordx2 v[20:21], v5, s[44:45]
	s_add_u32 s42, s42, 0x2000
	s_addc_u32 s43, s43, 0
	s_add_u32 s44, s44, 0x2000
	s_addc_u32 s45, s45, 0
	global_load_dwordx4 v[22:25], v4, s[42:43]
	global_load_dwordx2 v[26:27], v5, s[44:45]
	s_add_u32 s42, s42, 0x2000
	s_addc_u32 s43, s43, 0
	s_add_u32 s44, s44, 0x2000
	s_addc_u32 s45, s45, 0
	global_load_dwordx4 v[28:31], v4, s[42:43]
	global_load_dwordx2 v[32:33], v5, s[44:45]
	s_add_u32 s42, s42, 0x2000
	s_addc_u32 s43, s43, 0
	s_add_u32 s44, s44, 0x2000
	s_addc_u32 s45, s45, 0
	global_load_dwordx4 v[34:37], v4, s[42:43]
	global_load_dwordx2 v[38:39], v5, s[44:45]
	s_add_u32 s42, s42, 0x2000
	s_addc_u32 s43, s43, 0
	s_add_u32 s44, s44, 0x2000
	s_addc_u32 s45, s45, 0
	global_load_dwordx4 v[40:43], v4, s[42:43]
	global_load_dwordx2 v[44:45], v5, s[44:45]
	s_add_u32 s42, s42, 0x2000
	s_addc_u32 s43, s43, 0
	s_add_u32 s44, s44, 0x2000
	s_addc_u32 s45, s45, 0
	global_load_dwordx4 v[46:49], v4, s[42:43]
	global_load_dwordx2 v[50:51], v5, s[44:45]
	s_add_u32 s42, s42, 0x2000
	s_addc_u32 s43, s43, 0
	s_add_u32 s44, s44, 0x2000
	s_addc_u32 s45, s45, 0
	global_load_dwordx4 v[52:55], v4, s[42:43]
	global_load_dwordx2 v[56:57], v5, s[44:45]
	s_add_u32 s42, s42, 0x2000
	s_addc_u32 s43, s43, 0
	s_add_u32 s44, s44, 0x2000
	s_addc_u32 s45, s45, 0
	v_mov_b32_e32 v6, 0
	v_mov_b32_e32 v7, 0
	v_mov_b32_e32 v8, 0
	v_mov_b32_e32 v9, 0
	s_cmp_eq_u32 s1, 0
	s_cbranch_scc1 .Lp5_main
	s_lshl_b32 s6, s0, 19
	s_add_u32 s50, s70, 0x200000
	s_addc_u32 s51, s71, 0
	s_add_u32 s50, s50, s6
	s_addc_u32 s51, s51, 0
	s_add_u32 s52, s70, 0x400000
	s_addc_u32 s53, s71, 0
	s_add_u32 s52, s52, s6
	s_addc_u32 s53, s53, 0
	global_load_dwordx4 v[154:157], v4, s[50:51]
	global_load_dwordx4 v[158:161], v4, s[52:53]
	s_add_u32 s50, s50, 0x2000
	s_addc_u32 s51, s51, 0
	s_add_u32 s52, s52, 0x2000
	s_addc_u32 s53, s53, 0
	global_load_dwordx4 v[162:165], v4, s[50:51]
	global_load_dwordx4 v[166:169], v4, s[52:53]
	s_add_u32 s50, s50, 0x2000
	s_addc_u32 s51, s51, 0
	s_add_u32 s52, s52, 0x2000
	s_addc_u32 s53, s53, 0
	global_load_dwordx4 v[170:173], v4, s[50:51]
	global_load_dwordx4 v[174:177], v4, s[52:53]
	s_add_u32 s50, s50, 0x2000
	s_addc_u32 s51, s51, 0
	s_add_u32 s52, s52, 0x2000
	s_addc_u32 s53, s53, 0
	global_load_dwordx4 v[178:181], v4, s[50:51]
	global_load_dwordx4 v[182:185], v4, s[52:53]
	s_add_u32 s50, s50, 0x2000
	s_addc_u32 s51, s51, 0
	s_add_u32 s52, s52, 0x2000
	s_addc_u32 s53, s53, 0
	global_load_dwordx4 v[186:189], v4, s[50:51]
	global_load_dwordx4 v[190:193], v4, s[52:53]
	s_add_u32 s50, s50, 0x2000
	s_addc_u32 s51, s51, 0
	s_add_u32 s52, s52, 0x2000
	s_addc_u32 s53, s53, 0
	global_load_dwordx4 v[194:197], v4, s[50:51]
	global_load_dwordx4 v[198:201], v4, s[52:53]
	s_add_u32 s50, s50, 0x2000
	s_addc_u32 s51, s51, 0
	s_add_u32 s52, s52, 0x2000
	s_addc_u32 s53, s53, 0
	global_load_dwordx4 v[202:205], v4, s[50:51]
	global_load_dwordx4 v[206:209], v4, s[52:53]
	s_add_u32 s50, s50, 0x2000
	s_addc_u32 s51, s51, 0
	s_add_u32 s52, s52, 0x2000
	s_addc_u32 s53, s53, 0
	global_load_dwordx4 v[210:213], v4, s[50:51]
	global_load_dwordx4 v[214:217], v4, s[52:53]
	s_add_u32 s50, s50, 0x2000
	s_addc_u32 s51, s51, 0
	s_add_u32 s52, s52, 0x2000
	s_addc_u32 s53, s53, 0
	s_mov_b32 s7, 0
.Lp5_carry:
	s_waitcnt vmcnt(14)
	s_cmp_lt_u32 s7, s1
	s_cbranch_scc0 .Lp5_cskip0
	v_pk_fma_f32 v[6:7], v[6:7], v[154:155], v[158:159]
	v_pk_fma_f32 v[8:9], v[8:9], v[156:157], v[160:161]
.Lp5_cskip0:
	global_load_dwordx4 v[154:157], v4, s[50:51]
	global_load_dwordx4 v[158:161], v4, s[52:53]
	s_add_u32 s50, s50, 0x2000
	s_addc_u32 s51, s51, 0
	s_add_u32 s52, s52, 0x2000
	s_addc_u32 s53, s53, 0
	s_add_u32 s7, s7, 1
	s_waitcnt vmcnt(14)
	s_cmp_lt_u32 s7, s1
	s_cbranch_scc0 .Lp5_cskip1
	v_pk_fma_f32 v[6:7], v[6:7], v[162:163], v[166:167]
	v_pk_fma_f32 v[8:9], v[8:9], v[164:165], v[168:169]
.Lp5_cskip1:
	global_load_dwordx4 v[162:165], v4, s[50:51]
	global_load_dwordx4 v[166:169], v4, s[52:53]
	s_add_u32 s50, s50, 0x2000
	s_addc_u32 s51, s51, 0
	s_add_u32 s52, s52, 0x2000
	s_addc_u32 s53, s53, 0
	s_add_u32 s7, s7, 1
	s_waitcnt vmcnt(14)
	s_cmp_lt_u32 s7, s1
	s_cbranch_scc0 .Lp5_cskip2
	v_pk_fma_f32 v[6:7], v[6:7], v[170:171], v[174:175]
	v_pk_fma_f32 v[8:9], v[8:9], v[172:173], v[176:177]
.Lp5_cskip2:
	global_load_dwordx4 v[170:173], v4, s[50:51]
	global_load_dwordx4 v[174:177], v4, s[52:53]
	s_add_u32 s50, s50, 0x2000
	s_addc_u32 s51, s51, 0
	s_add_u32 s52, s52, 0x2000
	s_addc_u32 s53, s53, 0
	s_add_u32 s7, s7, 1
	s_waitcnt vmcnt(14)
	s_cmp_lt_u32 s7, s1
	s_cbranch_scc0 .Lp5_cskip3
	v_pk_fma_f32 v[6:7], v[6:7], v[178:179], v[182:183]
	v_pk_fma_f32 v[8:9], v[8:9], v[180:181], v[184:185]
; __device__ __forceinline__ unsigned cvtpk(float lo, float hi) { unsigned r; asm volatile("v_cvt_pk_bf16_f32 %0, %1, %2" : "=v"(r) : "v"(lo), "v"(hi)); return r; }
; __device__ __forceinline__ float bflo(unsigned w) { return __uint_as_float(w << 16); }
; __device__ __forceinline__ float bfhi(unsigned w) { return __uint_as_float(w & 0xffff0000u); }
; __device__ __forceinline__ float gelu_tanh(float x) { const float u = 1.5957691216057308f * (x + 0.044715f * x * x * x); return x * sigmoidf_(u); }
; __global__ void __launch_bounds__(NTHREADS, 2) fwd_kernel(Args args) {
;     ...
;             for (int c = 0; c < ch; ++c) { const f32x4 a = *(const f32x4*)(AGA + (size_t)(b * NCH + c) * D + 4 * tid), bb = *(const f32x4*)(AGB + (size_t)(b * NCH + c) * D + 4 * tid); h = a * h + bb; }
; #pragma unroll 8
;             for (int t = 0; t < SCH; ++t) {
;                 const u32x4 pw = *(const u32x4*)(AB + (r0 + t) * D + 4 * tid);
;                 const f32x4 a = {__builtin_amdgcn_exp2f(bflo(pw.x)), __builtin_amdgcn_exp2f(bflo(pw.y)), __builtin_amdgcn_exp2f(bflo(pw.z)), __builtin_amdgcn_exp2f(bflo(pw.w))};
;                 const f32x4 bb = {bfhi(pw.x), bfhi(pw.y), bfhi(pw.z), bfhi(pw.w)};
;                 const u32x2 gw2 = *(const u32x2*)(U + (r0 + t) * (2 * D) + 4 * tid);
;                 h = a * h + bb;
;                 const float y0 = h.x * gelu_tanh(bflo(gw2.x)), y1 = h.y * gelu_tanh(bfhi(gw2.x)), y2 = h.z * gelu_tanh(bflo(gw2.y)), y3 = h.w * gelu_tanh(bfhi(gw2.y));
;                 u32x2 w; w.x = cvtpk(y0, y1); w.y = cvtpk(y2, y3);
;                 *(u32x2*)(Y + (r0 + t) * D + 4 * tid) = w;
.Lp5_cskip3:
	global_load_dwordx4 v[178:181], v4, s[50:51]
	global_load_dwordx4 v[182:185], v4, s[52:53]
	s_add_u32 s50, s50, 0x2000
	s_addc_u32 s51, s51, 0
	s_add_u32 s52, s52, 0x2000
	s_addc_u32 s53, s53, 0
	s_add_u32 s7, s7, 1
	s_waitcnt vmcnt(14)
	s_cmp_lt_u32 s7, s1
	s_cbranch_scc0 .Lp5_cskip4
	v_pk_fma_f32 v[6:7], v[6:7], v[186:187], v[190:191]
	v_pk_fma_f32 v[8:9], v[8:9], v[188:189], v[192:193]
.Lp5_cskip4:
	global_load_dwordx4 v[186:189], v4, s[50:51]
	global_load_dwordx4 v[190:193], v4, s[52:53]
	s_add_u32 s50, s50, 0x2000
	s_addc_u32 s51, s51, 0
	s_add_u32 s52, s52, 0x2000
	s_addc_u32 s53, s53, 0
	s_add_u32 s7, s7, 1
	s_waitcnt vmcnt(14)
	s_cmp_lt_u32 s7, s1
	s_cbranch_scc0 .Lp5_cskip5
	v_pk_fma_f32 v[6:7], v[6:7], v[194:195], v[198:199]
	v_pk_fma_f32 v[8:9], v[8:9], v[196:197], v[200:201]
.Lp5_cskip5:
	global_load_dwordx4 v[194:197], v4, s[50:51]
	global_load_dwordx4 v[198:201], v4, s[52:53]
	s_add_u32 s50, s50, 0x2000
	s_addc_u32 s51, s51, 0
	s_add_u32 s52, s52, 0x2000
	s_addc_u32 s53, s53, 0
	s_add_u32 s7, s7, 1
	s_waitcnt vmcnt(14)
	s_cmp_lt_u32 s7, s1
	s_cbranch_scc0 .Lp5_cskip6
	v_pk_fma_f32 v[6:7], v[6:7], v[202:203], v[206:207]
	v_pk_fma_f32 v[8:9], v[8:9], v[204:205], v[208:209]
.Lp5_cskip6:
	global_load_dwordx4 v[202:205], v4, s[50:51]
	global_load_dwordx4 v[206:209], v4, s[52:53]
	s_add_u32 s50, s50, 0x2000
	s_addc_u32 s51, s51, 0
	s_add_u32 s52, s52, 0x2000
	s_addc_u32 s53, s53, 0
	s_add_u32 s7, s7, 1
	s_waitcnt vmcnt(14)
	s_cmp_lt_u32 s7, s1
	s_cbranch_scc0 .Lp5_cskip7
	v_pk_fma_f32 v[6:7], v[6:7], v[210:211], v[214:215]
	v_pk_fma_f32 v[8:9], v[8:9], v[212:213], v[216:217]
.Lp5_cskip7:
	global_load_dwordx4 v[210:213], v4, s[50:51]
	global_load_dwordx4 v[214:217], v4, s[52:53]
	s_add_u32 s50, s50, 0x2000
	s_addc_u32 s51, s51, 0
	s_add_u32 s52, s52, 0x2000
	s_addc_u32 s53, s53, 0
	s_add_u32 s7, s7, 1
	s_cmp_lt_u32 s7, s1
	s_cbranch_scc1 .Lp5_carry
.Lp5_main:
	s_waitcnt vmcnt(14)
	v_lshlrev_b32_e32 v78, 16, v10
	v_lshlrev_b32_e32 v79, 16, v11
	v_lshlrev_b32_e32 v80, 16, v12
	v_lshlrev_b32_e32 v81, 16, v13
	v_exp_f32_e32 v74, v78
	v_exp_f32_e32 v75, v79
	v_exp_f32_e32 v76, v80
	v_exp_f32_e32 v77, v81
	v_and_b32_e32 v10, 0xffff0000, v10
	v_and_b32_e32 v11, 0xffff0000, v11
	v_and_b32_e32 v12, 0xffff0000, v12
	v_and_b32_e32 v13, 0xffff0000, v13
	v_lshlrev_b32_e32 v82, 16, v14
	v_and_b32_e32 v83, 0xffff0000, v14
	v_lshlrev_b32_e32 v84, 16, v15
	v_and_b32_e32 v85, 0xffff0000, v15
	v_pk_fma_f32 v[6:7], v[6:7], v[74:75], v[10:11]
	v_pk_fma_f32 v[8:9], v[8:9], v[76:77], v[12:13]
	v_mul_f32_e32 v86, 0x3d372713, v82
	v_mul_f32_e32 v87, 0x3d372713, v83
	v_mul_f32_e32 v88, 0x3d372713, v84
	v_mul_f32_e32 v89, 0x3d372713, v85
	v_mul_f32_e32 v86, v86, v82
	v_mul_f32_e32 v87, v87, v83
	v_mul_f32_e32 v88, v88, v84
	v_mul_f32_e32 v89, v89, v85
	v_fma_f32 v86, v86, v82, v82
	v_fma_f32 v87, v87, v83, v83
	v_fma_f32 v88, v88, v84, v84
	v_fma_f32 v89, v89, v85, v85
	v_mul_f32_e32 v86, 0x3fcc422a, v86
	v_mul_f32_e32 v87, 0x3fcc422a, v87
	v_mul_f32_e32 v88, 0x3fcc422a, v88
	v_mul_f32_e32 v89, 0x3fcc422a, v89
	v_mul_f32_e32 v86, 0xbfb8aa3b, v86
	v_mul_f32_e32 v87, 0xbfb8aa3b, v87
	v_mul_f32_e32 v88, 0xbfb8aa3b, v88
	v_mul_f32_e32 v89, 0xbfb8aa3b, v89
	v_exp_f32_e32 v86, v86
	v_exp_f32_e32 v87, v87
	v_exp_f32_e32 v88, v88
	v_exp_f32_e32 v89, v89
	v_add_f32_e32 v86, 1.0, v86
	v_add_f32_e32 v87, 1.0, v87
	v_add_f32_e32 v88, 1.0, v88
	v_add_f32_e32 v89, 1.0, v89
	v_rcp_f32_e32 v86, v86
	v_rcp_f32_e32 v87, v87
	v_rcp_f32_e32 v88, v88
	v_rcp_f32_e32 v89, v89
	v_mul_f32_e32 v86, v86, v82
	v_mul_f32_e32 v87, v87, v83
	v_mul_f32_e32 v88, v88, v84
	v_mul_f32_e32 v89, v89, v85
	v_mul_f32_e32 v86, v6, v86
	v_mul_f32_e32 v87, v7, v87
	v_mul_f32_e32 v88, v8, v88
	v_mul_f32_e32 v89, v9, v89
	v_cvt_pk_bf16_f32 v58, v86, v87
	v_cvt_pk_bf16_f32 v59, v88, v89
	global_store_dwordx2 v5, v[58:59], s[46:47]
	s_add_u32 s46, s46, 0x1000
	s_addc_u32 s47, s47, 0
	global_load_dwordx4 v[10:13], v4, s[42:43]
	global_load_dwordx2 v[14:15], v5, s[44:45]
	s_add_u32 s42, s42, 0x2000
	s_addc_u32 s43, s43, 0
	s_add_u32 s44, s44, 0x2000
	s_addc_u32 s45, s45, 0
	s_waitcnt vmcnt(15)
	v_lshlrev_b32_e32 v78, 16, v16
	v_lshlrev_b32_e32 v79, 16, v17
	v_lshlrev_b32_e32 v80, 16, v18
	v_lshlrev_b32_e32 v81, 16, v19
	v_exp_f32_e32 v74, v78
	v_exp_f32_e32 v75, v79
	v_exp_f32_e32 v76, v80
	v_exp_f32_e32 v77, v81
	v_and_b32_e32 v16, 0xffff0000, v16
	v_and_b32_e32 v17, 0xffff0000, v17
	v_and_b32_e32 v18, 0xffff0000, v18
	v_and_b32_e32 v19, 0xffff0000, v19
	v_lshlrev_b32_e32 v82, 16, v20
	v_and_b32_e32 v83, 0xffff0000, v20
	v_lshlrev_b32_e32 v84, 16, v21
	v_and_b32_e32 v85, 0xffff0000, v21
	v_pk_fma_f32 v[6:7], v[6:7], v[74:75], v[16:17]
	v_pk_fma_f32 v[8:9], v[8:9], v[76:77], v[18:19]
	v_mul_f32_e32 v86, 0x3d372713, v82
	v_mul_f32_e32 v87, 0x3d372713, v83
	v_mul_f32_e32 v88, 0x3d372713, v84
	v_mul_f32_e32 v89, 0x3d372713, v85
	v_mul_f32_e32 v86, v86, v82
	v_mul_f32_e32 v87, v87, v83
	v_mul_f32_e32 v88, v88, v84
	v_mul_f32_e32 v89, v89, v85
	v_fma_f32 v86, v86, v82, v82
	v_fma_f32 v87, v87, v83, v83
	v_fma_f32 v88, v88, v84, v84
	v_fma_f32 v89, v89, v85, v85
	v_mul_f32_e32 v86, 0x3fcc422a, v86
	v_mul_f32_e32 v87, 0x3fcc422a, v87
	v_mul_f32_e32 v88, 0x3fcc422a, v88
	v_mul_f32_e32 v89, 0x3fcc422a, v89
	v_mul_f32_e32 v86, 0xbfb8aa3b, v86
	v_mul_f32_e32 v87, 0xbfb8aa3b, v87
	v_mul_f32_e32 v88, 0xbfb8aa3b, v88
	v_mul_f32_e32 v89, 0xbfb8aa3b, v89
	v_exp_f32_e32 v86, v86
	v_exp_f32_e32 v87, v87
	v_exp_f32_e32 v88, v88
	v_exp_f32_e32 v89, v89
	v_add_f32_e32 v86, 1.0, v86
	v_add_f32_e32 v87, 1.0, v87
	v_add_f32_e32 v88, 1.0, v88
	v_add_f32_e32 v89, 1.0, v89
	v_rcp_f32_e32 v86, v86
	v_rcp_f32_e32 v87, v87
	v_rcp_f32_e32 v88, v88
	v_rcp_f32_e32 v89, v89
	v_mul_f32_e32 v86, v86, v82
	v_mul_f32_e32 v87, v87, v83
	v_mul_f32_e32 v88, v88, v84
	v_mul_f32_e32 v89, v89, v85
	v_mul_f32_e32 v86, v6, v86
	v_mul_f32_e32 v87, v7, v87
	v_mul_f32_e32 v88, v8, v88
	v_mul_f32_e32 v89, v9, v89
	v_cvt_pk_bf16_f32 v60, v86, v87
	v_cvt_pk_bf16_f32 v61, v88, v89
	global_store_dwordx2 v5, v[60:61], s[46:47]
	s_add_u32 s46, s46, 0x1000
	s_addc_u32 s47, s47, 0
	global_load_dwordx4 v[16:19], v4, s[42:43]
	global_load_dwordx2 v[20:21], v5, s[44:45]
	s_add_u32 s42, s42, 0x2000
	s_addc_u32 s43, s43, 0
	s_add_u32 s44, s44, 0x2000
	s_addc_u32 s45, s45, 0
	s_waitcnt vmcnt(16)
; __device__ __forceinline__ unsigned cvtpk(float lo, float hi) { unsigned r; asm volatile("v_cvt_pk_bf16_f32 %0, %1, %2" : "=v"(r) : "v"(lo), "v"(hi)); return r; }
; __device__ __forceinline__ float bflo(unsigned w) { return __uint_as_float(w << 16); }
; __device__ __forceinline__ float bfhi(unsigned w) { return __uint_as_float(w & 0xffff0000u); }
; __device__ __forceinline__ float gelu_tanh(float x) { const float u = 1.5957691216057308f * (x + 0.044715f * x * x * x); return x * sigmoidf_(u); }
; __device__ __forceinline__ float sigmoidf_(float x) { return __builtin_amdgcn_rcpf(1.0f + __expf(-x)); }
; __global__ void __launch_bounds__(NTHREADS, 2) fwd_kernel(Args args) {
;     ...
;             for (int t = 0; t < SCH; ++t) {
;                 const u32x4 pw = *(const u32x4*)(AB + (r0 + t) * D + 4 * tid);
;                 const f32x4 a = {__builtin_amdgcn_exp2f(bflo(pw.x)), __builtin_amdgcn_exp2f(bflo(pw.y)), __builtin_amdgcn_exp2f(bflo(pw.z)), __builtin_amdgcn_exp2f(bflo(pw.w))};
;                 const f32x4 bb = {bfhi(pw.x), bfhi(pw.y), bfhi(pw.z), bfhi(pw.w)};
;                 const u32x2 gw2 = *(const u32x2*)(U + (r0 + t) * (2 * D) + 4 * tid);
;                 h = a * h + bb;
;                 const float y0 = h.x * gelu_tanh(bflo(gw2.x)), y1 = h.y * gelu_tanh(bfhi(gw2.x)), y2 = h.z * gelu_tanh(bflo(gw2.y)), y3 = h.w * gelu_tanh(bfhi(gw2.y));
;                 u32x2 w; w.x = cvtpk(y0, y1); w.y = cvtpk(y2, y3);
;                 *(u32x2*)(Y + (r0 + t) * D + 4 * tid) = w;
;             }
	v_lshlrev_b32_e32 v78, 16, v22
	v_lshlrev_b32_e32 v79, 16, v23
	v_lshlrev_b32_e32 v80, 16, v24
	v_lshlrev_b32_e32 v81, 16, v25
	v_exp_f32_e32 v74, v78
	v_exp_f32_e32 v75, v79
	v_exp_f32_e32 v76, v80
	v_exp_f32_e32 v77, v81
	v_and_b32_e32 v22, 0xffff0000, v22
	v_and_b32_e32 v23, 0xffff0000, v23
	v_and_b32_e32 v24, 0xffff0000, v24
	v_and_b32_e32 v25, 0xffff0000, v25
	v_lshlrev_b32_e32 v82, 16, v26
	v_and_b32_e32 v83, 0xffff0000, v26
	v_lshlrev_b32_e32 v84, 16, v27
	v_and_b32_e32 v85, 0xffff0000, v27
	v_pk_fma_f32 v[6:7], v[6:7], v[74:75], v[22:23]
	v_pk_fma_f32 v[8:9], v[8:9], v[76:77], v[24:25]
	v_mul_f32_e32 v86, 0x3d372713, v82
	v_mul_f32_e32 v87, 0x3d372713, v83
	v_mul_f32_e32 v88, 0x3d372713, v84
	v_mul_f32_e32 v89, 0x3d372713, v85
	v_mul_f32_e32 v86, v86, v82
	v_mul_f32_e32 v87, v87, v83
	v_mul_f32_e32 v88, v88, v84
	v_mul_f32_e32 v89, v89, v85
	v_fma_f32 v86, v86, v82, v82
	v_fma_f32 v87, v87, v83, v83
	v_fma_f32 v88, v88, v84, v84
	v_fma_f32 v89, v89, v85, v85
	v_mul_f32_e32 v86, 0x3fcc422a, v86
	v_mul_f32_e32 v87, 0x3fcc422a, v87
	v_mul_f32_e32 v88, 0x3fcc422a, v88
	v_mul_f32_e32 v89, 0x3fcc422a, v89
	v_mul_f32_e32 v86, 0xbfb8aa3b, v86
	v_mul_f32_e32 v87, 0xbfb8aa3b, v87
	v_mul_f32_e32 v88, 0xbfb8aa3b, v88
	v_mul_f32_e32 v89, 0xbfb8aa3b, v89
	v_exp_f32_e32 v86, v86
	v_exp_f32_e32 v87, v87
	v_exp_f32_e32 v88, v88
	v_exp_f32_e32 v89, v89
	v_add_f32_e32 v86, 1.0, v86
	v_add_f32_e32 v87, 1.0, v87
	v_add_f32_e32 v88, 1.0, v88
	v_add_f32_e32 v89, 1.0, v89
	v_rcp_f32_e32 v86, v86
	v_rcp_f32_e32 v87, v87
	v_rcp_f32_e32 v88, v88
	v_rcp_f32_e32 v89, v89
	v_mul_f32_e32 v86, v86, v82
	v_mul_f32_e32 v87, v87, v83
	v_mul_f32_e32 v88, v88, v84
	v_mul_f32_e32 v89, v89, v85
	v_mul_f32_e32 v86, v6, v86
	v_mul_f32_e32 v87, v7, v87
	v_mul_f32_e32 v88, v8, v88
	v_mul_f32_e32 v89, v9, v89
	v_cvt_pk_bf16_f32 v62, v86, v87
	v_cvt_pk_bf16_f32 v63, v88, v89
	global_store_dwordx2 v5, v[62:63], s[46:47]
	s_add_u32 s46, s46, 0x1000
	s_addc_u32 s47, s47, 0
	global_load_dwordx4 v[22:25], v4, s[42:43]
	global_load_dwordx2 v[26:27], v5, s[44:45]
	s_add_u32 s42, s42, 0x2000
	s_addc_u32 s43, s43, 0
	s_add_u32 s44, s44, 0x2000
	s_addc_u32 s45, s45, 0
	s_waitcnt vmcnt(17)
	v_lshlrev_b32_e32 v78, 16, v28
	v_lshlrev_b32_e32 v79, 16, v29
	v_lshlrev_b32_e32 v80, 16, v30
	v_lshlrev_b32_e32 v81, 16, v31
	v_exp_f32_e32 v74, v78
	v_exp_f32_e32 v75, v79
	v_exp_f32_e32 v76, v80
	v_exp_f32_e32 v77, v81
	v_and_b32_e32 v28, 0xffff0000, v28
	v_and_b32_e32 v29, 0xffff0000, v29
	v_and_b32_e32 v30, 0xffff0000, v30
	v_and_b32_e32 v31, 0xffff0000, v31
	v_lshlrev_b32_e32 v82, 16, v32
	v_and_b32_e32 v83, 0xffff0000, v32
	v_lshlrev_b32_e32 v84, 16, v33
	v_and_b32_e32 v85, 0xffff0000, v33
	v_pk_fma_f32 v[6:7], v[6:7], v[74:75], v[28:29]
	v_pk_fma_f32 v[8:9], v[8:9], v[76:77], v[30:31]
	v_mul_f32_e32 v86, 0x3d372713, v82
	v_mul_f32_e32 v87, 0x3d372713, v83
	v_mul_f32_e32 v88, 0x3d372713, v84
	v_mul_f32_e32 v89, 0x3d372713, v85
	v_mul_f32_e32 v86, v86, v82
	v_mul_f32_e32 v87, v87, v83
	v_mul_f32_e32 v88, v88, v84
	v_mul_f32_e32 v89, v89, v85
	v_fma_f32 v86, v86, v82, v82
	v_fma_f32 v87, v87, v83, v83
	v_fma_f32 v88, v88, v84, v84
	v_fma_f32 v89, v89, v85, v85
	v_mul_f32_e32 v86, 0x3fcc422a, v86
	v_mul_f32_e32 v87, 0x3fcc422a, v87
	v_mul_f32_e32 v88, 0x3fcc422a, v88
	v_mul_f32_e32 v89, 0x3fcc422a, v89
	v_mul_f32_e32 v86, 0xbfb8aa3b, v86
	v_mul_f32_e32 v87, 0xbfb8aa3b, v87
	v_mul_f32_e32 v88, 0xbfb8aa3b, v88
	v_mul_f32_e32 v89, 0xbfb8aa3b, v89
	v_exp_f32_e32 v86, v86
	v_exp_f32_e32 v87, v87
	v_exp_f32_e32 v88, v88
	v_exp_f32_e32 v89, v89
	v_add_f32_e32 v86, 1.0, v86
	v_add_f32_e32 v87, 1.0, v87
	v_add_f32_e32 v88, 1.0, v88
	v_add_f32_e32 v89, 1.0, v89
	v_rcp_f32_e32 v86, v86
	v_rcp_f32_e32 v87, v87
	v_rcp_f32_e32 v88, v88
	v_rcp_f32_e32 v89, v89
	v_mul_f32_e32 v86, v86, v82
	v_mul_f32_e32 v87, v87, v83
	v_mul_f32_e32 v88, v88, v84
	v_mul_f32_e32 v89, v89, v85
	v_mul_f32_e32 v86, v6, v86
	v_mul_f32_e32 v87, v7, v87
	v_mul_f32_e32 v88, v8, v88
	v_mul_f32_e32 v89, v9, v89
	v_cvt_pk_bf16_f32 v64, v86, v87
	v_cvt_pk_bf16_f32 v65, v88, v89
	global_store_dwordx2 v5, v[64:65], s[46:47]
	s_add_u32 s46, s46, 0x1000
	s_addc_u32 s47, s47, 0
	global_load_dwordx4 v[28:31], v4, s[42:43]
	global_load_dwordx2 v[32:33], v5, s[44:45]
	s_add_u32 s42, s42, 0x2000
	s_addc_u32 s43, s43, 0
	s_add_u32 s44, s44, 0x2000
	s_addc_u32 s45, s45, 0
	s_waitcnt vmcnt(18)
	v_lshlrev_b32_e32 v78, 16, v34
	v_lshlrev_b32_e32 v79, 16, v35
	v_lshlrev_b32_e32 v80, 16, v36
	v_lshlrev_b32_e32 v81, 16, v37
	v_exp_f32_e32 v74, v78
	v_exp_f32_e32 v75, v79
	v_exp_f32_e32 v76, v80
	v_exp_f32_e32 v77, v81
	v_and_b32_e32 v34, 0xffff0000, v34
	v_and_b32_e32 v35, 0xffff0000, v35
	v_and_b32_e32 v36, 0xffff0000, v36
	v_and_b32_e32 v37, 0xffff0000, v37
	v_lshlrev_b32_e32 v82, 16, v38
	v_and_b32_e32 v83, 0xffff0000, v38
	v_lshlrev_b32_e32 v84, 16, v39
	v_and_b32_e32 v85, 0xffff0000, v39
	v_pk_fma_f32 v[6:7], v[6:7], v[74:75], v[34:35]
	v_pk_fma_f32 v[8:9], v[8:9], v[76:77], v[36:37]
	v_mul_f32_e32 v86, 0x3d372713, v82
	v_mul_f32_e32 v87, 0x3d372713, v83
	v_mul_f32_e32 v88, 0x3d372713, v84
	v_mul_f32_e32 v89, 0x3d372713, v85
	v_mul_f32_e32 v86, v86, v82
	v_mul_f32_e32 v87, v87, v83
	v_mul_f32_e32 v88, v88, v84
	v_mul_f32_e32 v89, v89, v85
	v_fma_f32 v86, v86, v82, v82
	v_fma_f32 v87, v87, v83, v83
	v_fma_f32 v88, v88, v84, v84
	v_fma_f32 v89, v89, v85, v85
	v_mul_f32_e32 v86, 0x3fcc422a, v86
	v_mul_f32_e32 v87, 0x3fcc422a, v87
	v_mul_f32_e32 v88, 0x3fcc422a, v88
	v_mul_f32_e32 v89, 0x3fcc422a, v89
	v_mul_f32_e32 v86, 0xbfb8aa3b, v86
	v_mul_f32_e32 v87, 0xbfb8aa3b, v87
	v_mul_f32_e32 v88, 0xbfb8aa3b, v88
	v_mul_f32_e32 v89, 0xbfb8aa3b, v89
	v_exp_f32_e32 v86, v86
	v_exp_f32_e32 v87, v87
	v_exp_f32_e32 v88, v88
	v_exp_f32_e32 v89, v89
	v_add_f32_e32 v86, 1.0, v86
	v_add_f32_e32 v87, 1.0, v87
	v_add_f32_e32 v88, 1.0, v88
	v_add_f32_e32 v89, 1.0, v89
	v_rcp_f32_e32 v86, v86
	v_rcp_f32_e32 v87, v87
	v_rcp_f32_e32 v88, v88
	v_rcp_f32_e32 v89, v89
	v_mul_f32_e32 v86, v86, v82
	v_mul_f32_e32 v87, v87, v83
	v_mul_f32_e32 v88, v88, v84
	v_mul_f32_e32 v89, v89, v85
	v_mul_f32_e32 v86, v6, v86
	v_mul_f32_e32 v87, v7, v87
	v_mul_f32_e32 v88, v8, v88
	v_mul_f32_e32 v89, v9, v89
	v_cvt_pk_bf16_f32 v66, v86, v87
	v_cvt_pk_bf16_f32 v67, v88, v89
	global_store_dwordx2 v5, v[66:67], s[46:47]
	s_add_u32 s46, s46, 0x1000
	s_addc_u32 s47, s47, 0
	global_load_dwordx4 v[34:37], v4, s[42:43]
	global_load_dwordx2 v[38:39], v5, s[44:45]
	s_add_u32 s42, s42, 0x2000
	s_addc_u32 s43, s43, 0
	s_add_u32 s44, s44, 0x2000
	s_addc_u32 s45, s45, 0
	s_waitcnt vmcnt(19)
; __device__ __forceinline__ unsigned cvtpk(float lo, float hi) { unsigned r; asm volatile("v_cvt_pk_bf16_f32 %0, %1, %2" : "=v"(r) : "v"(lo), "v"(hi)); return r; }
; __device__ __forceinline__ float bflo(unsigned w) { return __uint_as_float(w << 16); }
; __device__ __forceinline__ float bfhi(unsigned w) { return __uint_as_float(w & 0xffff0000u); }
; __device__ __forceinline__ float gelu_tanh(float x) { const float u = 1.5957691216057308f * (x + 0.044715f * x * x * x); return x * sigmoidf_(u); }
; __device__ __forceinline__ float sigmoidf_(float x) { return __builtin_amdgcn_rcpf(1.0f + __expf(-x)); }
; __global__ void __launch_bounds__(NTHREADS, 2) fwd_kernel(Args args) {
;     ...
;             for (int t = 0; t < SCH; ++t) {
;                 const u32x4 pw = *(const u32x4*)(AB + (r0 + t) * D + 4 * tid);
;                 const f32x4 a = {__builtin_amdgcn_exp2f(bflo(pw.x)), __builtin_amdgcn_exp2f(bflo(pw.y)), __builtin_amdgcn_exp2f(bflo(pw.z)), __builtin_amdgcn_exp2f(bflo(pw.w))};
;                 const f32x4 bb = {bfhi(pw.x), bfhi(pw.y), bfhi(pw.z), bfhi(pw.w)};
;                 const u32x2 gw2 = *(const u32x2*)(U + (r0 + t) * (2 * D) + 4 * tid);
;                 h = a * h + bb;
;                 const float y0 = h.x * gelu_tanh(bflo(gw2.x)), y1 = h.y * gelu_tanh(bfhi(gw2.x)), y2 = h.z * gelu_tanh(bflo(gw2.y)), y3 = h.w * gelu_tanh(bfhi(gw2.y));
;                 u32x2 w; w.x = cvtpk(y0, y1); w.y = cvtpk(y2, y3);
;                 *(u32x2*)(Y + (r0 + t) * D + 4 * tid) = w;
;             }
	v_lshlrev_b32_e32 v78, 16, v40
	v_lshlrev_b32_e32 v79, 16, v41
	v_lshlrev_b32_e32 v80, 16, v42
	v_lshlrev_b32_e32 v81, 16, v43
	v_exp_f32_e32 v74, v78
	v_exp_f32_e32 v75, v79
	v_exp_f32_e32 v76, v80
	v_exp_f32_e32 v77, v81
	v_and_b32_e32 v40, 0xffff0000, v40
	v_and_b32_e32 v41, 0xffff0000, v41
	v_and_b32_e32 v42, 0xffff0000, v42
	v_and_b32_e32 v43, 0xffff0000, v43
	v_lshlrev_b32_e32 v82, 16, v44
	v_and_b32_e32 v83, 0xffff0000, v44
	v_lshlrev_b32_e32 v84, 16, v45
	v_and_b32_e32 v85, 0xffff0000, v45
	v_pk_fma_f32 v[6:7], v[6:7], v[74:75], v[40:41]
	v_pk_fma_f32 v[8:9], v[8:9], v[76:77], v[42:43]
	v_mul_f32_e32 v86, 0x3d372713, v82
	v_mul_f32_e32 v87, 0x3d372713, v83
	v_mul_f32_e32 v88, 0x3d372713, v84
	v_mul_f32_e32 v89, 0x3d372713, v85
	v_mul_f32_e32 v86, v86, v82
	v_mul_f32_e32 v87, v87, v83
	v_mul_f32_e32 v88, v88, v84
	v_mul_f32_e32 v89, v89, v85
	v_fma_f32 v86, v86, v82, v82
	v_fma_f32 v87, v87, v83, v83
	v_fma_f32 v88, v88, v84, v84
	v_fma_f32 v89, v89, v85, v85
	v_mul_f32_e32 v86, 0x3fcc422a, v86
	v_mul_f32_e32 v87, 0x3fcc422a, v87
	v_mul_f32_e32 v88, 0x3fcc422a, v88
	v_mul_f32_e32 v89, 0x3fcc422a, v89
	v_mul_f32_e32 v86, 0xbfb8aa3b, v86
	v_mul_f32_e32 v87, 0xbfb8aa3b, v87
	v_mul_f32_e32 v88, 0xbfb8aa3b, v88
	v_mul_f32_e32 v89, 0xbfb8aa3b, v89
	v_exp_f32_e32 v86, v86
	v_exp_f32_e32 v87, v87
	v_exp_f32_e32 v88, v88
	v_exp_f32_e32 v89, v89
	v_add_f32_e32 v86, 1.0, v86
	v_add_f32_e32 v87, 1.0, v87
	v_add_f32_e32 v88, 1.0, v88
	v_add_f32_e32 v89, 1.0, v89
	v_rcp_f32_e32 v86, v86
	v_rcp_f32_e32 v87, v87
	v_rcp_f32_e32 v88, v88
	v_rcp_f32_e32 v89, v89
	v_mul_f32_e32 v86, v86, v82
	v_mul_f32_e32 v87, v87, v83
	v_mul_f32_e32 v88, v88, v84
	v_mul_f32_e32 v89, v89, v85
	v_mul_f32_e32 v86, v6, v86
	v_mul_f32_e32 v87, v7, v87
	v_mul_f32_e32 v88, v8, v88
	v_mul_f32_e32 v89, v9, v89
	v_cvt_pk_bf16_f32 v68, v86, v87
	v_cvt_pk_bf16_f32 v69, v88, v89
	global_store_dwordx2 v5, v[68:69], s[46:47]
	s_add_u32 s46, s46, 0x1000
	s_addc_u32 s47, s47, 0
	global_load_dwordx4 v[40:43], v4, s[42:43]
	global_load_dwordx2 v[44:45], v5, s[44:45]
	s_add_u32 s42, s42, 0x2000
	s_addc_u32 s43, s43, 0
	s_add_u32 s44, s44, 0x2000
	s_addc_u32 s45, s45, 0
	s_waitcnt vmcnt(20)
	v_lshlrev_b32_e32 v78, 16, v46
	v_lshlrev_b32_e32 v79, 16, v47
	v_lshlrev_b32_e32 v80, 16, v48
	v_lshlrev_b32_e32 v81, 16, v49
	v_exp_f32_e32 v74, v78
	v_exp_f32_e32 v75, v79
	v_exp_f32_e32 v76, v80
	v_exp_f32_e32 v77, v81
	v_and_b32_e32 v46, 0xffff0000, v46
	v_and_b32_e32 v47, 0xffff0000, v47
	v_and_b32_e32 v48, 0xffff0000, v48
	v_and_b32_e32 v49, 0xffff0000, v49
	v_lshlrev_b32_e32 v82, 16, v50
	v_and_b32_e32 v83, 0xffff0000, v50
	v_lshlrev_b32_e32 v84, 16, v51
	v_and_b32_e32 v85, 0xffff0000, v51
	v_pk_fma_f32 v[6:7], v[6:7], v[74:75], v[46:47]
	v_pk_fma_f32 v[8:9], v[8:9], v[76:77], v[48:49]
	v_mul_f32_e32 v86, 0x3d372713, v82
	v_mul_f32_e32 v87, 0x3d372713, v83
	v_mul_f32_e32 v88, 0x3d372713, v84
	v_mul_f32_e32 v89, 0x3d372713, v85
	v_mul_f32_e32 v86, v86, v82
	v_mul_f32_e32 v87, v87, v83
	v_mul_f32_e32 v88, v88, v84
	v_mul_f32_e32 v89, v89, v85
	v_fma_f32 v86, v86, v82, v82
	v_fma_f32 v87, v87, v83, v83
	v_fma_f32 v88, v88, v84, v84
	v_fma_f32 v89, v89, v85, v85
	v_mul_f32_e32 v86, 0x3fcc422a, v86
	v_mul_f32_e32 v87, 0x3fcc422a, v87
	v_mul_f32_e32 v88, 0x3fcc422a, v88
	v_mul_f32_e32 v89, 0x3fcc422a, v89
	v_mul_f32_e32 v86, 0xbfb8aa3b, v86
	v_mul_f32_e32 v87, 0xbfb8aa3b, v87
	v_mul_f32_e32 v88, 0xbfb8aa3b, v88
	v_mul_f32_e32 v89, 0xbfb8aa3b, v89
	v_exp_f32_e32 v86, v86
	v_exp_f32_e32 v87, v87
	v_exp_f32_e32 v88, v88
	v_exp_f32_e32 v89, v89
	v_add_f32_e32 v86, 1.0, v86
	v_add_f32_e32 v87, 1.0, v87
	v_add_f32_e32 v88, 1.0, v88
	v_add_f32_e32 v89, 1.0, v89
	v_rcp_f32_e32 v86, v86
	v_rcp_f32_e32 v87, v87
	v_rcp_f32_e32 v88, v88
	v_rcp_f32_e32 v89, v89
	v_mul_f32_e32 v86, v86, v82
	v_mul_f32_e32 v87, v87, v83
	v_mul_f32_e32 v88, v88, v84
	v_mul_f32_e32 v89, v89, v85
	v_mul_f32_e32 v86, v6, v86
	v_mul_f32_e32 v87, v7, v87
	v_mul_f32_e32 v88, v8, v88
	v_mul_f32_e32 v89, v9, v89
	v_cvt_pk_bf16_f32 v70, v86, v87
	v_cvt_pk_bf16_f32 v71, v88, v89
	global_store_dwordx2 v5, v[70:71], s[46:47]
	s_add_u32 s46, s46, 0x1000
	s_addc_u32 s47, s47, 0
	global_load_dwordx4 v[46:49], v4, s[42:43]
	global_load_dwordx2 v[50:51], v5, s[44:45]
	s_add_u32 s42, s42, 0x2000
	s_addc_u32 s43, s43, 0
	s_add_u32 s44, s44, 0x2000
	s_addc_u32 s45, s45, 0
	s_waitcnt vmcnt(21)
	v_lshlrev_b32_e32 v78, 16, v52
	v_lshlrev_b32_e32 v79, 16, v53
	v_lshlrev_b32_e32 v80, 16, v54
	v_lshlrev_b32_e32 v81, 16, v55
	v_exp_f32_e32 v74, v78
	v_exp_f32_e32 v75, v79
	v_exp_f32_e32 v76, v80
	v_exp_f32_e32 v77, v81
	v_and_b32_e32 v52, 0xffff0000, v52
	v_and_b32_e32 v53, 0xffff0000, v53
	v_and_b32_e32 v54, 0xffff0000, v54
	v_and_b32_e32 v55, 0xffff0000, v55
	v_lshlrev_b32_e32 v82, 16, v56
	v_and_b32_e32 v83, 0xffff0000, v56
	v_lshlrev_b32_e32 v84, 16, v57
	v_and_b32_e32 v85, 0xffff0000, v57
	v_pk_fma_f32 v[6:7], v[6:7], v[74:75], v[52:53]
	v_pk_fma_f32 v[8:9], v[8:9], v[76:77], v[54:55]
	v_mul_f32_e32 v86, 0x3d372713, v82
	v_mul_f32_e32 v87, 0x3d372713, v83
	v_mul_f32_e32 v88, 0x3d372713, v84
	v_mul_f32_e32 v89, 0x3d372713, v85
	v_mul_f32_e32 v86, v86, v82
	v_mul_f32_e32 v87, v87, v83
	v_mul_f32_e32 v88, v88, v84
	v_mul_f32_e32 v89, v89, v85
	v_fma_f32 v86, v86, v82, v82
	v_fma_f32 v87, v87, v83, v83
	v_fma_f32 v88, v88, v84, v84
	v_fma_f32 v89, v89, v85, v85
	v_mul_f32_e32 v86, 0x3fcc422a, v86
	v_mul_f32_e32 v87, 0x3fcc422a, v87
	v_mul_f32_e32 v88, 0x3fcc422a, v88
	v_mul_f32_e32 v89, 0x3fcc422a, v89
	v_mul_f32_e32 v86, 0xbfb8aa3b, v86
	v_mul_f32_e32 v87, 0xbfb8aa3b, v87
	v_mul_f32_e32 v88, 0xbfb8aa3b, v88
	v_mul_f32_e32 v89, 0xbfb8aa3b, v89
	v_exp_f32_e32 v86, v86
	v_exp_f32_e32 v87, v87
	v_exp_f32_e32 v88, v88
	v_exp_f32_e32 v89, v89
	v_add_f32_e32 v86, 1.0, v86
	v_add_f32_e32 v87, 1.0, v87
	v_add_f32_e32 v88, 1.0, v88
	v_add_f32_e32 v89, 1.0, v89
	v_rcp_f32_e32 v86, v86
	v_rcp_f32_e32 v87, v87
	v_rcp_f32_e32 v88, v88
	v_rcp_f32_e32 v89, v89
	v_mul_f32_e32 v86, v86, v82
	v_mul_f32_e32 v87, v87, v83
	v_mul_f32_e32 v88, v88, v84
	v_mul_f32_e32 v89, v89, v85
	v_mul_f32_e32 v86, v6, v86
	v_mul_f32_e32 v87, v7, v87
	v_mul_f32_e32 v88, v8, v88
	v_mul_f32_e32 v89, v9, v89
	v_cvt_pk_bf16_f32 v72, v86, v87
	v_cvt_pk_bf16_f32 v73, v88, v89
	global_store_dwordx2 v5, v[72:73], s[46:47]
	s_add_u32 s46, s46, 0x1000
	s_addc_u32 s47, s47, 0
	global_load_dwordx4 v[52:55], v4, s[42:43]
	global_load_dwordx2 v[56:57], v5, s[44:45]
	s_add_u32 s42, s42, 0x2000
	s_addc_u32 s43, s43, 0
	s_add_u32 s44, s44, 0x2000
	s_addc_u32 s45, s45, 0
	s_mov_b32 s7, 6
; __device__ __forceinline__ unsigned cvtpk(float lo, float hi) { unsigned r; asm volatile("v_cvt_pk_bf16_f32 %0, %1, %2" : "=v"(r) : "v"(lo), "v"(hi)); return r; }
; __device__ __forceinline__ float bflo(unsigned w) { return __uint_as_float(w << 16); }
; __device__ __forceinline__ float bfhi(unsigned w) { return __uint_as_float(w & 0xffff0000u); }
; __device__ __forceinline__ float gelu_tanh(float x) { const float u = 1.5957691216057308f * (x + 0.044715f * x * x * x); return x * sigmoidf_(u); }
; __device__ __forceinline__ float sigmoidf_(float x) { return __builtin_amdgcn_rcpf(1.0f + __expf(-x)); }
; __global__ void __launch_bounds__(NTHREADS, 2) fwd_kernel(Args args) {
;     ...
;             for (int t = 0; t < SCH; ++t) {
;                 const u32x4 pw = *(const u32x4*)(AB + (r0 + t) * D + 4 * tid);
;                 const f32x4 a = {__builtin_amdgcn_exp2f(bflo(pw.x)), __builtin_amdgcn_exp2f(bflo(pw.y)), __builtin_amdgcn_exp2f(bflo(pw.z)), __builtin_amdgcn_exp2f(bflo(pw.w))};
;                 const f32x4 bb = {bfhi(pw.x), bfhi(pw.y), bfhi(pw.z), bfhi(pw.w)};
;                 const u32x2 gw2 = *(const u32x2*)(U + (r0 + t) * (2 * D) + 4 * tid);
;                 h = a * h + bb;
;                 const float y0 = h.x * gelu_tanh(bflo(gw2.x)), y1 = h.y * gelu_tanh(bfhi(gw2.x)), y2 = h.z * gelu_tanh(bflo(gw2.y)), y3 = h.w * gelu_tanh(bfhi(gw2.y));
;                 u32x2 w; w.x = cvtpk(y0, y1); w.y = cvtpk(y2, y3);
;                 *(u32x2*)(Y + (r0 + t) * D + 4 * tid) = w;
;             }
.Lp5_steady:
	s_waitcnt vmcnt(21)
	v_lshlrev_b32_e32 v78, 16, v10
	v_lshlrev_b32_e32 v79, 16, v11
	v_lshlrev_b32_e32 v80, 16, v12
	v_lshlrev_b32_e32 v81, 16, v13
	v_exp_f32_e32 v74, v78
	v_exp_f32_e32 v75, v79
	v_exp_f32_e32 v76, v80
	v_exp_f32_e32 v77, v81
	v_and_b32_e32 v10, 0xffff0000, v10
	v_and_b32_e32 v11, 0xffff0000, v11
	v_and_b32_e32 v12, 0xffff0000, v12
	v_and_b32_e32 v13, 0xffff0000, v13
	v_lshlrev_b32_e32 v82, 16, v14
	v_and_b32_e32 v83, 0xffff0000, v14
	v_lshlrev_b32_e32 v84, 16, v15
	v_and_b32_e32 v85, 0xffff0000, v15
	v_pk_fma_f32 v[6:7], v[6:7], v[74:75], v[10:11]
	v_pk_fma_f32 v[8:9], v[8:9], v[76:77], v[12:13]
	v_mul_f32_e32 v86, 0x3d372713, v82
	v_mul_f32_e32 v87, 0x3d372713, v83
	v_mul_f32_e32 v88, 0x3d372713, v84
	v_mul_f32_e32 v89, 0x3d372713, v85
	v_mul_f32_e32 v86, v86, v82
	v_mul_f32_e32 v87, v87, v83
	v_mul_f32_e32 v88, v88, v84
	v_mul_f32_e32 v89, v89, v85
	v_fma_f32 v86, v86, v82, v82
	v_fma_f32 v87, v87, v83, v83
	v_fma_f32 v88, v88, v84, v84
	v_fma_f32 v89, v89, v85, v85
	v_mul_f32_e32 v86, 0x3fcc422a, v86
	v_mul_f32_e32 v87, 0x3fcc422a, v87
	v_mul_f32_e32 v88, 0x3fcc422a, v88
	v_mul_f32_e32 v89, 0x3fcc422a, v89
	v_mul_f32_e32 v86, 0xbfb8aa3b, v86
	v_mul_f32_e32 v87, 0xbfb8aa3b, v87
	v_mul_f32_e32 v88, 0xbfb8aa3b, v88
	v_mul_f32_e32 v89, 0xbfb8aa3b, v89
	v_exp_f32_e32 v86, v86
	v_exp_f32_e32 v87, v87
	v_exp_f32_e32 v88, v88
	v_exp_f32_e32 v89, v89
	v_add_f32_e32 v86, 1.0, v86
	v_add_f32_e32 v87, 1.0, v87
	v_add_f32_e32 v88, 1.0, v88
	v_add_f32_e32 v89, 1.0, v89
	v_rcp_f32_e32 v86, v86
	v_rcp_f32_e32 v87, v87
	v_rcp_f32_e32 v88, v88
	v_rcp_f32_e32 v89, v89
	v_mul_f32_e32 v86, v86, v82
	v_mul_f32_e32 v87, v87, v83
	v_mul_f32_e32 v88, v88, v84
	v_mul_f32_e32 v89, v89, v85
	v_mul_f32_e32 v86, v6, v86
	v_mul_f32_e32 v87, v7, v87
	v_mul_f32_e32 v88, v8, v88
	v_mul_f32_e32 v89, v9, v89
	v_cvt_pk_bf16_f32 v58, v86, v87
	v_cvt_pk_bf16_f32 v59, v88, v89
	global_store_dwordx2 v5, v[58:59], s[46:47]
	s_add_u32 s46, s46, 0x1000
	s_addc_u32 s47, s47, 0
	global_load_dwordx4 v[10:13], v4, s[42:43]
	global_load_dwordx2 v[14:15], v5, s[44:45]
	s_add_u32 s42, s42, 0x2000
	s_addc_u32 s43, s43, 0
	s_add_u32 s44, s44, 0x2000
	s_addc_u32 s45, s45, 0
	s_waitcnt vmcnt(21)
	v_lshlrev_b32_e32 v78, 16, v16
	v_lshlrev_b32_e32 v79, 16, v17
	v_lshlrev_b32_e32 v80, 16, v18
	v_lshlrev_b32_e32 v81, 16, v19
	v_exp_f32_e32 v74, v78
	v_exp_f32_e32 v75, v79
	v_exp_f32_e32 v76, v80
	v_exp_f32_e32 v77, v81
	v_and_b32_e32 v16, 0xffff0000, v16
	v_and_b32_e32 v17, 0xffff0000, v17
	v_and_b32_e32 v18, 0xffff0000, v18
	v_and_b32_e32 v19, 0xffff0000, v19
	v_lshlrev_b32_e32 v82, 16, v20
	v_and_b32_e32 v83, 0xffff0000, v20
	v_lshlrev_b32_e32 v84, 16, v21
	v_and_b32_e32 v85, 0xffff0000, v21
	v_pk_fma_f32 v[6:7], v[6:7], v[74:75], v[16:17]
	v_pk_fma_f32 v[8:9], v[8:9], v[76:77], v[18:19]
	v_mul_f32_e32 v86, 0x3d372713, v82
	v_mul_f32_e32 v87, 0x3d372713, v83
	v_mul_f32_e32 v88, 0x3d372713, v84
	v_mul_f32_e32 v89, 0x3d372713, v85
	v_mul_f32_e32 v86, v86, v82
	v_mul_f32_e32 v87, v87, v83
	v_mul_f32_e32 v88, v88, v84
	v_mul_f32_e32 v89, v89, v85
	v_fma_f32 v86, v86, v82, v82
	v_fma_f32 v87, v87, v83, v83
	v_fma_f32 v88, v88, v84, v84
	v_fma_f32 v89, v89, v85, v85
	v_mul_f32_e32 v86, 0x3fcc422a, v86
	v_mul_f32_e32 v87, 0x3fcc422a, v87
	v_mul_f32_e32 v88, 0x3fcc422a, v88
	v_mul_f32_e32 v89, 0x3fcc422a, v89
	v_mul_f32_e32 v86, 0xbfb8aa3b, v86
	v_mul_f32_e32 v87, 0xbfb8aa3b, v87
	v_mul_f32_e32 v88, 0xbfb8aa3b, v88
	v_mul_f32_e32 v89, 0xbfb8aa3b, v89
	v_exp_f32_e32 v86, v86
	v_exp_f32_e32 v87, v87
	v_exp_f32_e32 v88, v88
	v_exp_f32_e32 v89, v89
	v_add_f32_e32 v86, 1.0, v86
	v_add_f32_e32 v87, 1.0, v87
	v_add_f32_e32 v88, 1.0, v88
	v_add_f32_e32 v89, 1.0, v89
	v_rcp_f32_e32 v86, v86
	v_rcp_f32_e32 v87, v87
	v_rcp_f32_e32 v88, v88
	v_rcp_f32_e32 v89, v89
	v_mul_f32_e32 v86, v86, v82
	v_mul_f32_e32 v87, v87, v83
	v_mul_f32_e32 v88, v88, v84
	v_mul_f32_e32 v89, v89, v85
	v_mul_f32_e32 v86, v6, v86
	v_mul_f32_e32 v87, v7, v87
	v_mul_f32_e32 v88, v8, v88
	v_mul_f32_e32 v89, v9, v89
	v_cvt_pk_bf16_f32 v60, v86, v87
	v_cvt_pk_bf16_f32 v61, v88, v89
	global_store_dwordx2 v5, v[60:61], s[46:47]
	s_add_u32 s46, s46, 0x1000
	s_addc_u32 s47, s47, 0
	global_load_dwordx4 v[16:19], v4, s[42:43]
	global_load_dwordx2 v[20:21], v5, s[44:45]
	s_add_u32 s42, s42, 0x2000
	s_addc_u32 s43, s43, 0
	s_add_u32 s44, s44, 0x2000
	s_addc_u32 s45, s45, 0
	s_waitcnt vmcnt(21)
	v_lshlrev_b32_e32 v78, 16, v22
	v_lshlrev_b32_e32 v79, 16, v23
	v_lshlrev_b32_e32 v80, 16, v24
	v_lshlrev_b32_e32 v81, 16, v25
	v_exp_f32_e32 v74, v78
	v_exp_f32_e32 v75, v79
	v_exp_f32_e32 v76, v80
	v_exp_f32_e32 v77, v81
	v_and_b32_e32 v22, 0xffff0000, v22
	v_and_b32_e32 v23, 0xffff0000, v23
	v_and_b32_e32 v24, 0xffff0000, v24
	v_and_b32_e32 v25, 0xffff0000, v25
	v_lshlrev_b32_e32 v82, 16, v26
	v_and_b32_e32 v83, 0xffff0000, v26
	v_lshlrev_b32_e32 v84, 16, v27
	v_and_b32_e32 v85, 0xffff0000, v27
	v_pk_fma_f32 v[6:7], v[6:7], v[74:75], v[22:23]
	v_pk_fma_f32 v[8:9], v[8:9], v[76:77], v[24:25]
	v_mul_f32_e32 v86, 0x3d372713, v82
	v_mul_f32_e32 v87, 0x3d372713, v83
	v_mul_f32_e32 v88, 0x3d372713, v84
	v_mul_f32_e32 v89, 0x3d372713, v85
	v_mul_f32_e32 v86, v86, v82
	v_mul_f32_e32 v87, v87, v83
	v_mul_f32_e32 v88, v88, v84
	v_mul_f32_e32 v89, v89, v85
	v_fma_f32 v86, v86, v82, v82
	v_fma_f32 v87, v87, v83, v83
	v_fma_f32 v88, v88, v84, v84
	v_fma_f32 v89, v89, v85, v85
	v_mul_f32_e32 v86, 0x3fcc422a, v86
	v_mul_f32_e32 v87, 0x3fcc422a, v87
	v_mul_f32_e32 v88, 0x3fcc422a, v88
	v_mul_f32_e32 v89, 0x3fcc422a, v89
	v_mul_f32_e32 v86, 0xbfb8aa3b, v86
	v_mul_f32_e32 v87, 0xbfb8aa3b, v87
	v_mul_f32_e32 v88, 0xbfb8aa3b, v88
	v_mul_f32_e32 v89, 0xbfb8aa3b, v89
	v_exp_f32_e32 v86, v86
	v_exp_f32_e32 v87, v87
	v_exp_f32_e32 v88, v88
	v_exp_f32_e32 v89, v89
	v_add_f32_e32 v86, 1.0, v86
	v_add_f32_e32 v87, 1.0, v87
	v_add_f32_e32 v88, 1.0, v88
	v_add_f32_e32 v89, 1.0, v89
	v_rcp_f32_e32 v86, v86
	v_rcp_f32_e32 v87, v87
	v_rcp_f32_e32 v88, v88
	v_rcp_f32_e32 v89, v89
	v_mul_f32_e32 v86, v86, v82
	v_mul_f32_e32 v87, v87, v83
	v_mul_f32_e32 v88, v88, v84
	v_mul_f32_e32 v89, v89, v85
	v_mul_f32_e32 v86, v6, v86
	v_mul_f32_e32 v87, v7, v87
	v_mul_f32_e32 v88, v8, v88
	v_mul_f32_e32 v89, v9, v89
	v_cvt_pk_bf16_f32 v62, v86, v87
	v_cvt_pk_bf16_f32 v63, v88, v89
	global_store_dwordx2 v5, v[62:63], s[46:47]
	s_add_u32 s46, s46, 0x1000
	s_addc_u32 s47, s47, 0
	global_load_dwordx4 v[22:25], v4, s[42:43]
	global_load_dwordx2 v[26:27], v5, s[44:45]
	s_add_u32 s42, s42, 0x2000
	s_addc_u32 s43, s43, 0
	s_add_u32 s44, s44, 0x2000
	s_addc_u32 s45, s45, 0
	s_waitcnt vmcnt(21)
; __device__ __forceinline__ unsigned cvtpk(float lo, float hi) { unsigned r; asm volatile("v_cvt_pk_bf16_f32 %0, %1, %2" : "=v"(r) : "v"(lo), "v"(hi)); return r; }
; __device__ __forceinline__ float bflo(unsigned w) { return __uint_as_float(w << 16); }
; __device__ __forceinline__ float bfhi(unsigned w) { return __uint_as_float(w & 0xffff0000u); }
; __device__ __forceinline__ float gelu_tanh(float x) { const float u = 1.5957691216057308f * (x + 0.044715f * x * x * x); return x * sigmoidf_(u); }
; __device__ __forceinline__ float sigmoidf_(float x) { return __builtin_amdgcn_rcpf(1.0f + __expf(-x)); }
; __global__ void __launch_bounds__(NTHREADS, 2) fwd_kernel(Args args) {
;     ...
;             for (int t = 0; t < SCH; ++t) {
;                 const u32x4 pw = *(const u32x4*)(AB + (r0 + t) * D + 4 * tid);
;                 const f32x4 a = {__builtin_amdgcn_exp2f(bflo(pw.x)), __builtin_amdgcn_exp2f(bflo(pw.y)), __builtin_amdgcn_exp2f(bflo(pw.z)), __builtin_amdgcn_exp2f(bflo(pw.w))};
;                 const f32x4 bb = {bfhi(pw.x), bfhi(pw.y), bfhi(pw.z), bfhi(pw.w)};
;                 const u32x2 gw2 = *(const u32x2*)(U + (r0 + t) * (2 * D) + 4 * tid);
;                 h = a * h + bb;
;                 const float y0 = h.x * gelu_tanh(bflo(gw2.x)), y1 = h.y * gelu_tanh(bfhi(gw2.x)), y2 = h.z * gelu_tanh(bflo(gw2.y)), y3 = h.w * gelu_tanh(bfhi(gw2.y));
;                 u32x2 w; w.x = cvtpk(y0, y1); w.y = cvtpk(y2, y3);
;                 *(u32x2*)(Y + (r0 + t) * D + 4 * tid) = w;
;             }
	v_lshlrev_b32_e32 v78, 16, v28
	v_lshlrev_b32_e32 v79, 16, v29
	v_lshlrev_b32_e32 v80, 16, v30
	v_lshlrev_b32_e32 v81, 16, v31
	v_exp_f32_e32 v74, v78
	v_exp_f32_e32 v75, v79
	v_exp_f32_e32 v76, v80
	v_exp_f32_e32 v77, v81
	v_and_b32_e32 v28, 0xffff0000, v28
	v_and_b32_e32 v29, 0xffff0000, v29
	v_and_b32_e32 v30, 0xffff0000, v30
	v_and_b32_e32 v31, 0xffff0000, v31
	v_lshlrev_b32_e32 v82, 16, v32
	v_and_b32_e32 v83, 0xffff0000, v32
	v_lshlrev_b32_e32 v84, 16, v33
	v_and_b32_e32 v85, 0xffff0000, v33
	v_pk_fma_f32 v[6:7], v[6:7], v[74:75], v[28:29]
	v_pk_fma_f32 v[8:9], v[8:9], v[76:77], v[30:31]
	v_mul_f32_e32 v86, 0x3d372713, v82
	v_mul_f32_e32 v87, 0x3d372713, v83
	v_mul_f32_e32 v88, 0x3d372713, v84
	v_mul_f32_e32 v89, 0x3d372713, v85
	v_mul_f32_e32 v86, v86, v82
	v_mul_f32_e32 v87, v87, v83
	v_mul_f32_e32 v88, v88, v84
	v_mul_f32_e32 v89, v89, v85
	v_fma_f32 v86, v86, v82, v82
	v_fma_f32 v87, v87, v83, v83
	v_fma_f32 v88, v88, v84, v84
	v_fma_f32 v89, v89, v85, v85
	v_mul_f32_e32 v86, 0x3fcc422a, v86
	v_mul_f32_e32 v87, 0x3fcc422a, v87
	v_mul_f32_e32 v88, 0x3fcc422a, v88
	v_mul_f32_e32 v89, 0x3fcc422a, v89
	v_mul_f32_e32 v86, 0xbfb8aa3b, v86
	v_mul_f32_e32 v87, 0xbfb8aa3b, v87
	v_mul_f32_e32 v88, 0xbfb8aa3b, v88
	v_mul_f32_e32 v89, 0xbfb8aa3b, v89
	v_exp_f32_e32 v86, v86
	v_exp_f32_e32 v87, v87
	v_exp_f32_e32 v88, v88
	v_exp_f32_e32 v89, v89
	v_add_f32_e32 v86, 1.0, v86
	v_add_f32_e32 v87, 1.0, v87
	v_add_f32_e32 v88, 1.0, v88
	v_add_f32_e32 v89, 1.0, v89
	v_rcp_f32_e32 v86, v86
	v_rcp_f32_e32 v87, v87
	v_rcp_f32_e32 v88, v88
	v_rcp_f32_e32 v89, v89
	v_mul_f32_e32 v86, v86, v82
	v_mul_f32_e32 v87, v87, v83
	v_mul_f32_e32 v88, v88, v84
	v_mul_f32_e32 v89, v89, v85
	v_mul_f32_e32 v86, v6, v86
	v_mul_f32_e32 v87, v7, v87
	v_mul_f32_e32 v88, v8, v88
	v_mul_f32_e32 v89, v9, v89
	v_cvt_pk_bf16_f32 v64, v86, v87
	v_cvt_pk_bf16_f32 v65, v88, v89
	global_store_dwordx2 v5, v[64:65], s[46:47]
	s_add_u32 s46, s46, 0x1000
	s_addc_u32 s47, s47, 0
	global_load_dwordx4 v[28:31], v4, s[42:43]
	global_load_dwordx2 v[32:33], v5, s[44:45]
	s_add_u32 s42, s42, 0x2000
	s_addc_u32 s43, s43, 0
	s_add_u32 s44, s44, 0x2000
	s_addc_u32 s45, s45, 0
	s_waitcnt vmcnt(21)
	v_lshlrev_b32_e32 v78, 16, v34
	v_lshlrev_b32_e32 v79, 16, v35
	v_lshlrev_b32_e32 v80, 16, v36
	v_lshlrev_b32_e32 v81, 16, v37
	v_exp_f32_e32 v74, v78
	v_exp_f32_e32 v75, v79
	v_exp_f32_e32 v76, v80
	v_exp_f32_e32 v77, v81
	v_and_b32_e32 v34, 0xffff0000, v34
	v_and_b32_e32 v35, 0xffff0000, v35
	v_and_b32_e32 v36, 0xffff0000, v36
	v_and_b32_e32 v37, 0xffff0000, v37
	v_lshlrev_b32_e32 v82, 16, v38
	v_and_b32_e32 v83, 0xffff0000, v38
	v_lshlrev_b32_e32 v84, 16, v39
	v_and_b32_e32 v85, 0xffff0000, v39
	v_pk_fma_f32 v[6:7], v[6:7], v[74:75], v[34:35]
	v_pk_fma_f32 v[8:9], v[8:9], v[76:77], v[36:37]
	v_mul_f32_e32 v86, 0x3d372713, v82
	v_mul_f32_e32 v87, 0x3d372713, v83
	v_mul_f32_e32 v88, 0x3d372713, v84
	v_mul_f32_e32 v89, 0x3d372713, v85
	v_mul_f32_e32 v86, v86, v82
	v_mul_f32_e32 v87, v87, v83
	v_mul_f32_e32 v88, v88, v84
	v_mul_f32_e32 v89, v89, v85
	v_fma_f32 v86, v86, v82, v82
	v_fma_f32 v87, v87, v83, v83
	v_fma_f32 v88, v88, v84, v84
	v_fma_f32 v89, v89, v85, v85
	v_mul_f32_e32 v86, 0x3fcc422a, v86
	v_mul_f32_e32 v87, 0x3fcc422a, v87
	v_mul_f32_e32 v88, 0x3fcc422a, v88
	v_mul_f32_e32 v89, 0x3fcc422a, v89
	v_mul_f32_e32 v86, 0xbfb8aa3b, v86
	v_mul_f32_e32 v87, 0xbfb8aa3b, v87
	v_mul_f32_e32 v88, 0xbfb8aa3b, v88
	v_mul_f32_e32 v89, 0xbfb8aa3b, v89
	v_exp_f32_e32 v86, v86
	v_exp_f32_e32 v87, v87
	v_exp_f32_e32 v88, v88
	v_exp_f32_e32 v89, v89
	v_add_f32_e32 v86, 1.0, v86
	v_add_f32_e32 v87, 1.0, v87
	v_add_f32_e32 v88, 1.0, v88
	v_add_f32_e32 v89, 1.0, v89
	v_rcp_f32_e32 v86, v86
	v_rcp_f32_e32 v87, v87
	v_rcp_f32_e32 v88, v88
	v_rcp_f32_e32 v89, v89
	v_mul_f32_e32 v86, v86, v82
	v_mul_f32_e32 v87, v87, v83
	v_mul_f32_e32 v88, v88, v84
	v_mul_f32_e32 v89, v89, v85
	v_mul_f32_e32 v86, v6, v86
	v_mul_f32_e32 v87, v7, v87
	v_mul_f32_e32 v88, v8, v88
	v_mul_f32_e32 v89, v9, v89
	v_cvt_pk_bf16_f32 v66, v86, v87
	v_cvt_pk_bf16_f32 v67, v88, v89
	global_store_dwordx2 v5, v[66:67], s[46:47]
	s_add_u32 s46, s46, 0x1000
	s_addc_u32 s47, s47, 0
	global_load_dwordx4 v[34:37], v4, s[42:43]
	global_load_dwordx2 v[38:39], v5, s[44:45]
	s_add_u32 s42, s42, 0x2000
	s_addc_u32 s43, s43, 0
	s_add_u32 s44, s44, 0x2000
	s_addc_u32 s45, s45, 0
	s_waitcnt vmcnt(21)
	v_lshlrev_b32_e32 v78, 16, v40
	v_lshlrev_b32_e32 v79, 16, v41
	v_lshlrev_b32_e32 v80, 16, v42
	v_lshlrev_b32_e32 v81, 16, v43
	v_exp_f32_e32 v74, v78
	v_exp_f32_e32 v75, v79
	v_exp_f32_e32 v76, v80
	v_exp_f32_e32 v77, v81
	v_and_b32_e32 v40, 0xffff0000, v40
	v_and_b32_e32 v41, 0xffff0000, v41
	v_and_b32_e32 v42, 0xffff0000, v42
	v_and_b32_e32 v43, 0xffff0000, v43
	v_lshlrev_b32_e32 v82, 16, v44
	v_and_b32_e32 v83, 0xffff0000, v44
	v_lshlrev_b32_e32 v84, 16, v45
	v_and_b32_e32 v85, 0xffff0000, v45
	v_pk_fma_f32 v[6:7], v[6:7], v[74:75], v[40:41]
	v_pk_fma_f32 v[8:9], v[8:9], v[76:77], v[42:43]
	v_mul_f32_e32 v86, 0x3d372713, v82
	v_mul_f32_e32 v87, 0x3d372713, v83
	v_mul_f32_e32 v88, 0x3d372713, v84
	v_mul_f32_e32 v89, 0x3d372713, v85
	v_mul_f32_e32 v86, v86, v82
	v_mul_f32_e32 v87, v87, v83
	v_mul_f32_e32 v88, v88, v84
	v_mul_f32_e32 v89, v89, v85
	v_fma_f32 v86, v86, v82, v82
	v_fma_f32 v87, v87, v83, v83
	v_fma_f32 v88, v88, v84, v84
	v_fma_f32 v89, v89, v85, v85
	v_mul_f32_e32 v86, 0x3fcc422a, v86
	v_mul_f32_e32 v87, 0x3fcc422a, v87
	v_mul_f32_e32 v88, 0x3fcc422a, v88
	v_mul_f32_e32 v89, 0x3fcc422a, v89
	v_mul_f32_e32 v86, 0xbfb8aa3b, v86
	v_mul_f32_e32 v87, 0xbfb8aa3b, v87
	v_mul_f32_e32 v88, 0xbfb8aa3b, v88
	v_mul_f32_e32 v89, 0xbfb8aa3b, v89
	v_exp_f32_e32 v86, v86
	v_exp_f32_e32 v87, v87
	v_exp_f32_e32 v88, v88
	v_exp_f32_e32 v89, v89
	v_add_f32_e32 v86, 1.0, v86
	v_add_f32_e32 v87, 1.0, v87
	v_add_f32_e32 v88, 1.0, v88
	v_add_f32_e32 v89, 1.0, v89
	v_rcp_f32_e32 v86, v86
	v_rcp_f32_e32 v87, v87
	v_rcp_f32_e32 v88, v88
	v_rcp_f32_e32 v89, v89
	v_mul_f32_e32 v86, v86, v82
	v_mul_f32_e32 v87, v87, v83
	v_mul_f32_e32 v88, v88, v84
	v_mul_f32_e32 v89, v89, v85
	v_mul_f32_e32 v86, v6, v86
	v_mul_f32_e32 v87, v7, v87
	v_mul_f32_e32 v88, v8, v88
	v_mul_f32_e32 v89, v9, v89
	v_cvt_pk_bf16_f32 v68, v86, v87
	v_cvt_pk_bf16_f32 v69, v88, v89
	global_store_dwordx2 v5, v[68:69], s[46:47]
	s_add_u32 s46, s46, 0x1000
	s_addc_u32 s47, s47, 0
	global_load_dwordx4 v[40:43], v4, s[42:43]
	global_load_dwordx2 v[44:45], v5, s[44:45]
	s_add_u32 s42, s42, 0x2000
	s_addc_u32 s43, s43, 0
	s_add_u32 s44, s44, 0x2000
	s_addc_u32 s45, s45, 0
	s_waitcnt vmcnt(21)
; __device__ __forceinline__ unsigned cvtpk(float lo, float hi) { unsigned r; asm volatile("v_cvt_pk_bf16_f32 %0, %1, %2" : "=v"(r) : "v"(lo), "v"(hi)); return r; }
; __device__ __forceinline__ float bflo(unsigned w) { return __uint_as_float(w << 16); }
; __device__ __forceinline__ float bfhi(unsigned w) { return __uint_as_float(w & 0xffff0000u); }
; __device__ __forceinline__ float gelu_tanh(float x) { const float u = 1.5957691216057308f * (x + 0.044715f * x * x * x); return x * sigmoidf_(u); }
; __device__ __forceinline__ float sigmoidf_(float x) { return __builtin_amdgcn_rcpf(1.0f + __expf(-x)); }
; __global__ void __launch_bounds__(NTHREADS, 2) fwd_kernel(Args args) {
;     ...
;             for (int t = 0; t < SCH; ++t) {
;                 const u32x4 pw = *(const u32x4*)(AB + (r0 + t) * D + 4 * tid);
;                 const f32x4 a = {__builtin_amdgcn_exp2f(bflo(pw.x)), __builtin_amdgcn_exp2f(bflo(pw.y)), __builtin_amdgcn_exp2f(bflo(pw.z)), __builtin_amdgcn_exp2f(bflo(pw.w))};
;                 const f32x4 bb = {bfhi(pw.x), bfhi(pw.y), bfhi(pw.z), bfhi(pw.w)};
;                 const u32x2 gw2 = *(const u32x2*)(U + (r0 + t) * (2 * D) + 4 * tid);
;                 h = a * h + bb;
;                 const float y0 = h.x * gelu_tanh(bflo(gw2.x)), y1 = h.y * gelu_tanh(bfhi(gw2.x)), y2 = h.z * gelu_tanh(bflo(gw2.y)), y3 = h.w * gelu_tanh(bfhi(gw2.y));
;                 u32x2 w; w.x = cvtpk(y0, y1); w.y = cvtpk(y2, y3);
;                 *(u32x2*)(Y + (r0 + t) * D + 4 * tid) = w;
;             }
	v_lshlrev_b32_e32 v78, 16, v46
	v_lshlrev_b32_e32 v79, 16, v47
	v_lshlrev_b32_e32 v80, 16, v48
	v_lshlrev_b32_e32 v81, 16, v49
	v_exp_f32_e32 v74, v78
	v_exp_f32_e32 v75, v79
	v_exp_f32_e32 v76, v80
	v_exp_f32_e32 v77, v81
	v_and_b32_e32 v46, 0xffff0000, v46
	v_and_b32_e32 v47, 0xffff0000, v47
	v_and_b32_e32 v48, 0xffff0000, v48
	v_and_b32_e32 v49, 0xffff0000, v49
	v_lshlrev_b32_e32 v82, 16, v50
	v_and_b32_e32 v83, 0xffff0000, v50
	v_lshlrev_b32_e32 v84, 16, v51
	v_and_b32_e32 v85, 0xffff0000, v51
	v_pk_fma_f32 v[6:7], v[6:7], v[74:75], v[46:47]
	v_pk_fma_f32 v[8:9], v[8:9], v[76:77], v[48:49]
	v_mul_f32_e32 v86, 0x3d372713, v82
	v_mul_f32_e32 v87, 0x3d372713, v83
	v_mul_f32_e32 v88, 0x3d372713, v84
	v_mul_f32_e32 v89, 0x3d372713, v85
	v_mul_f32_e32 v86, v86, v82
	v_mul_f32_e32 v87, v87, v83
	v_mul_f32_e32 v88, v88, v84
	v_mul_f32_e32 v89, v89, v85
	v_fma_f32 v86, v86, v82, v82
	v_fma_f32 v87, v87, v83, v83
	v_fma_f32 v88, v88, v84, v84
	v_fma_f32 v89, v89, v85, v85
	v_mul_f32_e32 v86, 0x3fcc422a, v86
	v_mul_f32_e32 v87, 0x3fcc422a, v87
	v_mul_f32_e32 v88, 0x3fcc422a, v88
	v_mul_f32_e32 v89, 0x3fcc422a, v89
	v_mul_f32_e32 v86, 0xbfb8aa3b, v86
	v_mul_f32_e32 v87, 0xbfb8aa3b, v87
	v_mul_f32_e32 v88, 0xbfb8aa3b, v88
	v_mul_f32_e32 v89, 0xbfb8aa3b, v89
	v_exp_f32_e32 v86, v86
	v_exp_f32_e32 v87, v87
	v_exp_f32_e32 v88, v88
	v_exp_f32_e32 v89, v89
	v_add_f32_e32 v86, 1.0, v86
	v_add_f32_e32 v87, 1.0, v87
	v_add_f32_e32 v88, 1.0, v88
	v_add_f32_e32 v89, 1.0, v89
	v_rcp_f32_e32 v86, v86
	v_rcp_f32_e32 v87, v87
	v_rcp_f32_e32 v88, v88
	v_rcp_f32_e32 v89, v89
	v_mul_f32_e32 v86, v86, v82
	v_mul_f32_e32 v87, v87, v83
	v_mul_f32_e32 v88, v88, v84
	v_mul_f32_e32 v89, v89, v85
	v_mul_f32_e32 v86, v6, v86
	v_mul_f32_e32 v87, v7, v87
	v_mul_f32_e32 v88, v8, v88
	v_mul_f32_e32 v89, v9, v89
	v_cvt_pk_bf16_f32 v70, v86, v87
	v_cvt_pk_bf16_f32 v71, v88, v89
	global_store_dwordx2 v5, v[70:71], s[46:47]
	s_add_u32 s46, s46, 0x1000
	s_addc_u32 s47, s47, 0
	global_load_dwordx4 v[46:49], v4, s[42:43]
	global_load_dwordx2 v[50:51], v5, s[44:45]
	s_add_u32 s42, s42, 0x2000
	s_addc_u32 s43, s43, 0
	s_add_u32 s44, s44, 0x2000
	s_addc_u32 s45, s45, 0
	s_waitcnt vmcnt(21)
	v_lshlrev_b32_e32 v78, 16, v52
	v_lshlrev_b32_e32 v79, 16, v53
	v_lshlrev_b32_e32 v80, 16, v54
	v_lshlrev_b32_e32 v81, 16, v55
	v_exp_f32_e32 v74, v78
	v_exp_f32_e32 v75, v79
	v_exp_f32_e32 v76, v80
	v_exp_f32_e32 v77, v81
	v_and_b32_e32 v52, 0xffff0000, v52
	v_and_b32_e32 v53, 0xffff0000, v53
	v_and_b32_e32 v54, 0xffff0000, v54
	v_and_b32_e32 v55, 0xffff0000, v55
	v_lshlrev_b32_e32 v82, 16, v56
	v_and_b32_e32 v83, 0xffff0000, v56
	v_lshlrev_b32_e32 v84, 16, v57
	v_and_b32_e32 v85, 0xffff0000, v57
	v_pk_fma_f32 v[6:7], v[6:7], v[74:75], v[52:53]
	v_pk_fma_f32 v[8:9], v[8:9], v[76:77], v[54:55]
	v_mul_f32_e32 v86, 0x3d372713, v82
	v_mul_f32_e32 v87, 0x3d372713, v83
	v_mul_f32_e32 v88, 0x3d372713, v84
	v_mul_f32_e32 v89, 0x3d372713, v85
	v_mul_f32_e32 v86, v86, v82
	v_mul_f32_e32 v87, v87, v83
	v_mul_f32_e32 v88, v88, v84
	v_mul_f32_e32 v89, v89, v85
	v_fma_f32 v86, v86, v82, v82
	v_fma_f32 v87, v87, v83, v83
	v_fma_f32 v88, v88, v84, v84
	v_fma_f32 v89, v89, v85, v85
	v_mul_f32_e32 v86, 0x3fcc422a, v86
	v_mul_f32_e32 v87, 0x3fcc422a, v87
	v_mul_f32_e32 v88, 0x3fcc422a, v88
	v_mul_f32_e32 v89, 0x3fcc422a, v89
	v_mul_f32_e32 v86, 0xbfb8aa3b, v86
	v_mul_f32_e32 v87, 0xbfb8aa3b, v87
	v_mul_f32_e32 v88, 0xbfb8aa3b, v88
	v_mul_f32_e32 v89, 0xbfb8aa3b, v89
	v_exp_f32_e32 v86, v86
	v_exp_f32_e32 v87, v87
	v_exp_f32_e32 v88, v88
	v_exp_f32_e32 v89, v89
	v_add_f32_e32 v86, 1.0, v86
	v_add_f32_e32 v87, 1.0, v87
	v_add_f32_e32 v88, 1.0, v88
	v_add_f32_e32 v89, 1.0, v89
	v_rcp_f32_e32 v86, v86
	v_rcp_f32_e32 v87, v87
	v_rcp_f32_e32 v88, v88
	v_rcp_f32_e32 v89, v89
	v_mul_f32_e32 v86, v86, v82
	v_mul_f32_e32 v87, v87, v83
	v_mul_f32_e32 v88, v88, v84
	v_mul_f32_e32 v89, v89, v85
	v_mul_f32_e32 v86, v6, v86
	v_mul_f32_e32 v87, v7, v87
	v_mul_f32_e32 v88, v8, v88
	v_mul_f32_e32 v89, v9, v89
	v_cvt_pk_bf16_f32 v72, v86, v87
	v_cvt_pk_bf16_f32 v73, v88, v89
	global_store_dwordx2 v5, v[72:73], s[46:47]
	s_add_u32 s46, s46, 0x1000
	s_addc_u32 s47, s47, 0
	global_load_dwordx4 v[52:55], v4, s[42:43]
	global_load_dwordx2 v[56:57], v5, s[44:45]
	s_add_u32 s42, s42, 0x2000
	s_addc_u32 s43, s43, 0
	s_add_u32 s44, s44, 0x2000
	s_addc_u32 s45, s45, 0
	s_sub_u32 s7, s7, 1
	s_cmp_lg_u32 s7, 0
	s_cbranch_scc1 .Lp5_steady
; __device__ __forceinline__ unsigned cvtpk(float lo, float hi) { unsigned r; asm volatile("v_cvt_pk_bf16_f32 %0, %1, %2" : "=v"(r) : "v"(lo), "v"(hi)); return r; }
; __device__ __forceinline__ float bflo(unsigned w) { return __uint_as_float(w << 16); }
; __device__ __forceinline__ float bfhi(unsigned w) { return __uint_as_float(w & 0xffff0000u); }
; __device__ __forceinline__ float gelu_tanh(float x) { const float u = 1.5957691216057308f * (x + 0.044715f * x * x * x); return x * sigmoidf_(u); }
; __device__ __forceinline__ float sigmoidf_(float x) { return __builtin_amdgcn_rcpf(1.0f + __expf(-x)); }
; __global__ void __launch_bounds__(NTHREADS, 2) fwd_kernel(Args args) {
;     ...
;             for (int t = 0; t < SCH; ++t) {
;                 const u32x4 pw = *(const u32x4*)(AB + (r0 + t) * D + 4 * tid);
;                 const f32x4 a = {__builtin_amdgcn_exp2f(bflo(pw.x)), __builtin_amdgcn_exp2f(bflo(pw.y)), __builtin_amdgcn_exp2f(bflo(pw.z)), __builtin_amdgcn_exp2f(bflo(pw.w))};
;                 const f32x4 bb = {bfhi(pw.x), bfhi(pw.y), bfhi(pw.z), bfhi(pw.w)};
;                 const u32x2 gw2 = *(const u32x2*)(U + (r0 + t) * (2 * D) + 4 * tid);
;                 h = a * h + bb;
;                 const float y0 = h.x * gelu_tanh(bflo(gw2.x)), y1 = h.y * gelu_tanh(bfhi(gw2.x)), y2 = h.z * gelu_tanh(bflo(gw2.y)), y3 = h.w * gelu_tanh(bfhi(gw2.y));
;                 u32x2 w; w.x = cvtpk(y0, y1); w.y = cvtpk(y2, y3);
;                 *(u32x2*)(Y + (r0 + t) * D + 4 * tid) = w;
;             }
	s_waitcnt vmcnt(21)
	v_lshlrev_b32_e32 v78, 16, v10
	v_lshlrev_b32_e32 v79, 16, v11
	v_lshlrev_b32_e32 v80, 16, v12
	v_lshlrev_b32_e32 v81, 16, v13
	v_exp_f32_e32 v74, v78
	v_exp_f32_e32 v75, v79
	v_exp_f32_e32 v76, v80
	v_exp_f32_e32 v77, v81
	v_and_b32_e32 v10, 0xffff0000, v10
	v_and_b32_e32 v11, 0xffff0000, v11
	v_and_b32_e32 v12, 0xffff0000, v12
	v_and_b32_e32 v13, 0xffff0000, v13
	v_lshlrev_b32_e32 v82, 16, v14
	v_and_b32_e32 v83, 0xffff0000, v14
	v_lshlrev_b32_e32 v84, 16, v15
	v_and_b32_e32 v85, 0xffff0000, v15
	v_pk_fma_f32 v[6:7], v[6:7], v[74:75], v[10:11]
	v_pk_fma_f32 v[8:9], v[8:9], v[76:77], v[12:13]
	v_mul_f32_e32 v86, 0x3d372713, v82
	v_mul_f32_e32 v87, 0x3d372713, v83
	v_mul_f32_e32 v88, 0x3d372713, v84
	v_mul_f32_e32 v89, 0x3d372713, v85
	v_mul_f32_e32 v86, v86, v82
	v_mul_f32_e32 v87, v87, v83
	v_mul_f32_e32 v88, v88, v84
	v_mul_f32_e32 v89, v89, v85
	v_fma_f32 v86, v86, v82, v82
	v_fma_f32 v87, v87, v83, v83
	v_fma_f32 v88, v88, v84, v84
	v_fma_f32 v89, v89, v85, v85
	v_mul_f32_e32 v86, 0x3fcc422a, v86
	v_mul_f32_e32 v87, 0x3fcc422a, v87
	v_mul_f32_e32 v88, 0x3fcc422a, v88
	v_mul_f32_e32 v89, 0x3fcc422a, v89
	v_mul_f32_e32 v86, 0xbfb8aa3b, v86
	v_mul_f32_e32 v87, 0xbfb8aa3b, v87
	v_mul_f32_e32 v88, 0xbfb8aa3b, v88
	v_mul_f32_e32 v89, 0xbfb8aa3b, v89
	v_exp_f32_e32 v86, v86
	v_exp_f32_e32 v87, v87
	v_exp_f32_e32 v88, v88
	v_exp_f32_e32 v89, v89
	v_add_f32_e32 v86, 1.0, v86
	v_add_f32_e32 v87, 1.0, v87
	v_add_f32_e32 v88, 1.0, v88
	v_add_f32_e32 v89, 1.0, v89
	v_rcp_f32_e32 v86, v86
	v_rcp_f32_e32 v87, v87
	v_rcp_f32_e32 v88, v88
	v_rcp_f32_e32 v89, v89
	v_mul_f32_e32 v86, v86, v82
	v_mul_f32_e32 v87, v87, v83
	v_mul_f32_e32 v88, v88, v84
	v_mul_f32_e32 v89, v89, v85
	v_mul_f32_e32 v86, v6, v86
	v_mul_f32_e32 v87, v7, v87
	v_mul_f32_e32 v88, v8, v88
	v_mul_f32_e32 v89, v9, v89
	v_cvt_pk_bf16_f32 v58, v86, v87
	v_cvt_pk_bf16_f32 v59, v88, v89
	global_store_dwordx2 v5, v[58:59], s[46:47]
	s_add_u32 s46, s46, 0x1000
	s_addc_u32 s47, s47, 0
	s_waitcnt vmcnt(19)
	v_lshlrev_b32_e32 v78, 16, v16
	v_lshlrev_b32_e32 v79, 16, v17
	v_lshlrev_b32_e32 v80, 16, v18
	v_lshlrev_b32_e32 v81, 16, v19
	v_exp_f32_e32 v74, v78
	v_exp_f32_e32 v75, v79
	v_exp_f32_e32 v76, v80
	v_exp_f32_e32 v77, v81
	v_and_b32_e32 v16, 0xffff0000, v16
	v_and_b32_e32 v17, 0xffff0000, v17
	v_and_b32_e32 v18, 0xffff0000, v18
	v_and_b32_e32 v19, 0xffff0000, v19
	v_lshlrev_b32_e32 v82, 16, v20
	v_and_b32_e32 v83, 0xffff0000, v20
	v_lshlrev_b32_e32 v84, 16, v21
	v_and_b32_e32 v85, 0xffff0000, v21
	v_pk_fma_f32 v[6:7], v[6:7], v[74:75], v[16:17]
	v_pk_fma_f32 v[8:9], v[8:9], v[76:77], v[18:19]
	v_mul_f32_e32 v86, 0x3d372713, v82
	v_mul_f32_e32 v87, 0x3d372713, v83
	v_mul_f32_e32 v88, 0x3d372713, v84
	v_mul_f32_e32 v89, 0x3d372713, v85
	v_mul_f32_e32 v86, v86, v82
	v_mul_f32_e32 v87, v87, v83
	v_mul_f32_e32 v88, v88, v84
	v_mul_f32_e32 v89, v89, v85
	v_fma_f32 v86, v86, v82, v82
	v_fma_f32 v87, v87, v83, v83
	v_fma_f32 v88, v88, v84, v84
	v_fma_f32 v89, v89, v85, v85
	v_mul_f32_e32 v86, 0x3fcc422a, v86
	v_mul_f32_e32 v87, 0x3fcc422a, v87
	v_mul_f32_e32 v88, 0x3fcc422a, v88
	v_mul_f32_e32 v89, 0x3fcc422a, v89
	v_mul_f32_e32 v86, 0xbfb8aa3b, v86
	v_mul_f32_e32 v87, 0xbfb8aa3b, v87
	v_mul_f32_e32 v88, 0xbfb8aa3b, v88
	v_mul_f32_e32 v89, 0xbfb8aa3b, v89
	v_exp_f32_e32 v86, v86
	v_exp_f32_e32 v87, v87
	v_exp_f32_e32 v88, v88
	v_exp_f32_e32 v89, v89
	v_add_f32_e32 v86, 1.0, v86
	v_add_f32_e32 v87, 1.0, v87
	v_add_f32_e32 v88, 1.0, v88
	v_add_f32_e32 v89, 1.0, v89
	v_rcp_f32_e32 v86, v86
	v_rcp_f32_e32 v87, v87
	v_rcp_f32_e32 v88, v88
	v_rcp_f32_e32 v89, v89
	v_mul_f32_e32 v86, v86, v82
	v_mul_f32_e32 v87, v87, v83
	v_mul_f32_e32 v88, v88, v84
	v_mul_f32_e32 v89, v89, v85
	v_mul_f32_e32 v86, v6, v86
	v_mul_f32_e32 v87, v7, v87
	v_mul_f32_e32 v88, v8, v88
	v_mul_f32_e32 v89, v9, v89
	v_cvt_pk_bf16_f32 v60, v86, v87
	v_cvt_pk_bf16_f32 v61, v88, v89
	global_store_dwordx2 v5, v[60:61], s[46:47]
	s_add_u32 s46, s46, 0x1000
	s_addc_u32 s47, s47, 0
	s_waitcnt vmcnt(17)
	v_lshlrev_b32_e32 v78, 16, v22
	v_lshlrev_b32_e32 v79, 16, v23
	v_lshlrev_b32_e32 v80, 16, v24
	v_lshlrev_b32_e32 v81, 16, v25
	v_exp_f32_e32 v74, v78
	v_exp_f32_e32 v75, v79
	v_exp_f32_e32 v76, v80
	v_exp_f32_e32 v77, v81
	v_and_b32_e32 v22, 0xffff0000, v22
	v_and_b32_e32 v23, 0xffff0000, v23
	v_and_b32_e32 v24, 0xffff0000, v24
	v_and_b32_e32 v25, 0xffff0000, v25
	v_lshlrev_b32_e32 v82, 16, v26
	v_and_b32_e32 v83, 0xffff0000, v26
	v_lshlrev_b32_e32 v84, 16, v27
	v_and_b32_e32 v85, 0xffff0000, v27
	v_pk_fma_f32 v[6:7], v[6:7], v[74:75], v[22:23]
	v_pk_fma_f32 v[8:9], v[8:9], v[76:77], v[24:25]
	v_mul_f32_e32 v86, 0x3d372713, v82
	v_mul_f32_e32 v87, 0x3d372713, v83
	v_mul_f32_e32 v88, 0x3d372713, v84
	v_mul_f32_e32 v89, 0x3d372713, v85
	v_mul_f32_e32 v86, v86, v82
	v_mul_f32_e32 v87, v87, v83
	v_mul_f32_e32 v88, v88, v84
	v_mul_f32_e32 v89, v89, v85
	v_fma_f32 v86, v86, v82, v82
	v_fma_f32 v87, v87, v83, v83
	v_fma_f32 v88, v88, v84, v84
	v_fma_f32 v89, v89, v85, v85
	v_mul_f32_e32 v86, 0x3fcc422a, v86
	v_mul_f32_e32 v87, 0x3fcc422a, v87
	v_mul_f32_e32 v88, 0x3fcc422a, v88
	v_mul_f32_e32 v89, 0x3fcc422a, v89
	v_mul_f32_e32 v86, 0xbfb8aa3b, v86
	v_mul_f32_e32 v87, 0xbfb8aa3b, v87
	v_mul_f32_e32 v88, 0xbfb8aa3b, v88
	v_mul_f32_e32 v89, 0xbfb8aa3b, v89
	v_exp_f32_e32 v86, v86
	v_exp_f32_e32 v87, v87
	v_exp_f32_e32 v88, v88
	v_exp_f32_e32 v89, v89
	v_add_f32_e32 v86, 1.0, v86
	v_add_f32_e32 v87, 1.0, v87
	v_add_f32_e32 v88, 1.0, v88
	v_add_f32_e32 v89, 1.0, v89
	v_rcp_f32_e32 v86, v86
	v_rcp_f32_e32 v87, v87
	v_rcp_f32_e32 v88, v88
	v_rcp_f32_e32 v89, v89
	v_mul_f32_e32 v86, v86, v82
	v_mul_f32_e32 v87, v87, v83
	v_mul_f32_e32 v88, v88, v84
	v_mul_f32_e32 v89, v89, v85
	v_mul_f32_e32 v86, v6, v86
	v_mul_f32_e32 v87, v7, v87
	v_mul_f32_e32 v88, v8, v88
	v_mul_f32_e32 v89, v9, v89
	v_cvt_pk_bf16_f32 v62, v86, v87
	v_cvt_pk_bf16_f32 v63, v88, v89
	global_store_dwordx2 v5, v[62:63], s[46:47]
	s_add_u32 s46, s46, 0x1000
	s_addc_u32 s47, s47, 0
	s_waitcnt vmcnt(15)
; __device__ __forceinline__ unsigned cvtpk(float lo, float hi) { unsigned r; asm volatile("v_cvt_pk_bf16_f32 %0, %1, %2" : "=v"(r) : "v"(lo), "v"(hi)); return r; }
; __device__ __forceinline__ float bflo(unsigned w) { return __uint_as_float(w << 16); }
; __device__ __forceinline__ float bfhi(unsigned w) { return __uint_as_float(w & 0xffff0000u); }
; __device__ __forceinline__ float gelu_tanh(float x) { const float u = 1.5957691216057308f * (x + 0.044715f * x * x * x); return x * sigmoidf_(u); }
; __device__ __forceinline__ float sigmoidf_(float x) { return __builtin_amdgcn_rcpf(1.0f + __expf(-x)); }
; __global__ void __launch_bounds__(NTHREADS, 2) fwd_kernel(Args args) {
;     ...
;             for (int t = 0; t < SCH; ++t) {
;                 const u32x4 pw = *(const u32x4*)(AB + (r0 + t) * D + 4 * tid);
;                 const f32x4 a = {__builtin_amdgcn_exp2f(bflo(pw.x)), __builtin_amdgcn_exp2f(bflo(pw.y)), __builtin_amdgcn_exp2f(bflo(pw.z)), __builtin_amdgcn_exp2f(bflo(pw.w))};
;                 const f32x4 bb = {bfhi(pw.x), bfhi(pw.y), bfhi(pw.z), bfhi(pw.w)};
;                 const u32x2 gw2 = *(const u32x2*)(U + (r0 + t) * (2 * D) + 4 * tid);
;                 h = a * h + bb;
;                 const float y0 = h.x * gelu_tanh(bflo(gw2.x)), y1 = h.y * gelu_tanh(bfhi(gw2.x)), y2 = h.z * gelu_tanh(bflo(gw2.y)), y3 = h.w * gelu_tanh(bfhi(gw2.y));
;                 u32x2 w; w.x = cvtpk(y0, y1); w.y = cvtpk(y2, y3);
;                 *(u32x2*)(Y + (r0 + t) * D + 4 * tid) = w;
;             }
	v_lshlrev_b32_e32 v78, 16, v28
	v_lshlrev_b32_e32 v79, 16, v29
	v_lshlrev_b32_e32 v80, 16, v30
	v_lshlrev_b32_e32 v81, 16, v31
	v_exp_f32_e32 v74, v78
	v_exp_f32_e32 v75, v79
	v_exp_f32_e32 v76, v80
	v_exp_f32_e32 v77, v81
	v_and_b32_e32 v28, 0xffff0000, v28
	v_and_b32_e32 v29, 0xffff0000, v29
	v_and_b32_e32 v30, 0xffff0000, v30
	v_and_b32_e32 v31, 0xffff0000, v31
	v_lshlrev_b32_e32 v82, 16, v32
	v_and_b32_e32 v83, 0xffff0000, v32
	v_lshlrev_b32_e32 v84, 16, v33
	v_and_b32_e32 v85, 0xffff0000, v33
	v_pk_fma_f32 v[6:7], v[6:7], v[74:75], v[28:29]
	v_pk_fma_f32 v[8:9], v[8:9], v[76:77], v[30:31]
	v_mul_f32_e32 v86, 0x3d372713, v82
	v_mul_f32_e32 v87, 0x3d372713, v83
	v_mul_f32_e32 v88, 0x3d372713, v84
	v_mul_f32_e32 v89, 0x3d372713, v85
	v_mul_f32_e32 v86, v86, v82
	v_mul_f32_e32 v87, v87, v83
	v_mul_f32_e32 v88, v88, v84
	v_mul_f32_e32 v89, v89, v85
	v_fma_f32 v86, v86, v82, v82
	v_fma_f32 v87, v87, v83, v83
	v_fma_f32 v88, v88, v84, v84
	v_fma_f32 v89, v89, v85, v85
	v_mul_f32_e32 v86, 0x3fcc422a, v86
	v_mul_f32_e32 v87, 0x3fcc422a, v87
	v_mul_f32_e32 v88, 0x3fcc422a, v88
	v_mul_f32_e32 v89, 0x3fcc422a, v89
	v_mul_f32_e32 v86, 0xbfb8aa3b, v86
	v_mul_f32_e32 v87, 0xbfb8aa3b, v87
	v_mul_f32_e32 v88, 0xbfb8aa3b, v88
	v_mul_f32_e32 v89, 0xbfb8aa3b, v89
	v_exp_f32_e32 v86, v86
	v_exp_f32_e32 v87, v87
	v_exp_f32_e32 v88, v88
	v_exp_f32_e32 v89, v89
	v_add_f32_e32 v86, 1.0, v86
	v_add_f32_e32 v87, 1.0, v87
	v_add_f32_e32 v88, 1.0, v88
	v_add_f32_e32 v89, 1.0, v89
	v_rcp_f32_e32 v86, v86
	v_rcp_f32_e32 v87, v87
	v_rcp_f32_e32 v88, v88
	v_rcp_f32_e32 v89, v89
	v_mul_f32_e32 v86, v86, v82
	v_mul_f32_e32 v87, v87, v83
	v_mul_f32_e32 v88, v88, v84
	v_mul_f32_e32 v89, v89, v85
	v_mul_f32_e32 v86, v6, v86
	v_mul_f32_e32 v87, v7, v87
	v_mul_f32_e32 v88, v8, v88
	v_mul_f32_e32 v89, v9, v89
	v_cvt_pk_bf16_f32 v64, v86, v87
	v_cvt_pk_bf16_f32 v65, v88, v89
	global_store_dwordx2 v5, v[64:65], s[46:47]
	s_add_u32 s46, s46, 0x1000
	s_addc_u32 s47, s47, 0
	s_waitcnt vmcnt(13)
	v_lshlrev_b32_e32 v78, 16, v34
	v_lshlrev_b32_e32 v79, 16, v35
	v_lshlrev_b32_e32 v80, 16, v36
	v_lshlrev_b32_e32 v81, 16, v37
	v_exp_f32_e32 v74, v78
	v_exp_f32_e32 v75, v79
	v_exp_f32_e32 v76, v80
	v_exp_f32_e32 v77, v81
	v_and_b32_e32 v34, 0xffff0000, v34
	v_and_b32_e32 v35, 0xffff0000, v35
	v_and_b32_e32 v36, 0xffff0000, v36
	v_and_b32_e32 v37, 0xffff0000, v37
	v_lshlrev_b32_e32 v82, 16, v38
	v_and_b32_e32 v83, 0xffff0000, v38
	v_lshlrev_b32_e32 v84, 16, v39
	v_and_b32_e32 v85, 0xffff0000, v39
	v_pk_fma_f32 v[6:7], v[6:7], v[74:75], v[34:35]
	v_pk_fma_f32 v[8:9], v[8:9], v[76:77], v[36:37]
	v_mul_f32_e32 v86, 0x3d372713, v82
	v_mul_f32_e32 v87, 0x3d372713, v83
	v_mul_f32_e32 v88, 0x3d372713, v84
	v_mul_f32_e32 v89, 0x3d372713, v85
	v_mul_f32_e32 v86, v86, v82
	v_mul_f32_e32 v87, v87, v83
	v_mul_f32_e32 v88, v88, v84
	v_mul_f32_e32 v89, v89, v85
	v_fma_f32 v86, v86, v82, v82
	v_fma_f32 v87, v87, v83, v83
	v_fma_f32 v88, v88, v84, v84
	v_fma_f32 v89, v89, v85, v85
	v_mul_f32_e32 v86, 0x3fcc422a, v86
	v_mul_f32_e32 v87, 0x3fcc422a, v87
	v_mul_f32_e32 v88, 0x3fcc422a, v88
	v_mul_f32_e32 v89, 0x3fcc422a, v89
	v_mul_f32_e32 v86, 0xbfb8aa3b, v86
	v_mul_f32_e32 v87, 0xbfb8aa3b, v87
	v_mul_f32_e32 v88, 0xbfb8aa3b, v88
	v_mul_f32_e32 v89, 0xbfb8aa3b, v89
	v_exp_f32_e32 v86, v86
	v_exp_f32_e32 v87, v87
	v_exp_f32_e32 v88, v88
	v_exp_f32_e32 v89, v89
	v_add_f32_e32 v86, 1.0, v86
	v_add_f32_e32 v87, 1.0, v87
	v_add_f32_e32 v88, 1.0, v88
	v_add_f32_e32 v89, 1.0, v89
	v_rcp_f32_e32 v86, v86
	v_rcp_f32_e32 v87, v87
	v_rcp_f32_e32 v88, v88
	v_rcp_f32_e32 v89, v89
	v_mul_f32_e32 v86, v86, v82
	v_mul_f32_e32 v87, v87, v83
	v_mul_f32_e32 v88, v88, v84
	v_mul_f32_e32 v89, v89, v85
	v_mul_f32_e32 v86, v6, v86
	v_mul_f32_e32 v87, v7, v87
	v_mul_f32_e32 v88, v8, v88
	v_mul_f32_e32 v89, v9, v89
	v_cvt_pk_bf16_f32 v66, v86, v87
	v_cvt_pk_bf16_f32 v67, v88, v89
	global_store_dwordx2 v5, v[66:67], s[46:47]
	s_add_u32 s46, s46, 0x1000
	s_addc_u32 s47, s47, 0
	s_waitcnt vmcnt(11)
	v_lshlrev_b32_e32 v78, 16, v40
	v_lshlrev_b32_e32 v79, 16, v41
	v_lshlrev_b32_e32 v80, 16, v42
	v_lshlrev_b32_e32 v81, 16, v43
	v_exp_f32_e32 v74, v78
	v_exp_f32_e32 v75, v79
	v_exp_f32_e32 v76, v80
	v_exp_f32_e32 v77, v81
	v_and_b32_e32 v40, 0xffff0000, v40
	v_and_b32_e32 v41, 0xffff0000, v41
	v_and_b32_e32 v42, 0xffff0000, v42
	v_and_b32_e32 v43, 0xffff0000, v43
	v_lshlrev_b32_e32 v82, 16, v44
	v_and_b32_e32 v83, 0xffff0000, v44
	v_lshlrev_b32_e32 v84, 16, v45
	v_and_b32_e32 v85, 0xffff0000, v45
	v_pk_fma_f32 v[6:7], v[6:7], v[74:75], v[40:41]
	v_pk_fma_f32 v[8:9], v[8:9], v[76:77], v[42:43]
	v_mul_f32_e32 v86, 0x3d372713, v82
	v_mul_f32_e32 v87, 0x3d372713, v83
	v_mul_f32_e32 v88, 0x3d372713, v84
	v_mul_f32_e32 v89, 0x3d372713, v85
	v_mul_f32_e32 v86, v86, v82
	v_mul_f32_e32 v87, v87, v83
	v_mul_f32_e32 v88, v88, v84
	v_mul_f32_e32 v89, v89, v85
	v_fma_f32 v86, v86, v82, v82
	v_fma_f32 v87, v87, v83, v83
	v_fma_f32 v88, v88, v84, v84
	v_fma_f32 v89, v89, v85, v85
	v_mul_f32_e32 v86, 0x3fcc422a, v86
	v_mul_f32_e32 v87, 0x3fcc422a, v87
	v_mul_f32_e32 v88, 0x3fcc422a, v88
	v_mul_f32_e32 v89, 0x3fcc422a, v89
	v_mul_f32_e32 v86, 0xbfb8aa3b, v86
	v_mul_f32_e32 v87, 0xbfb8aa3b, v87
	v_mul_f32_e32 v88, 0xbfb8aa3b, v88
	v_mul_f32_e32 v89, 0xbfb8aa3b, v89
	v_exp_f32_e32 v86, v86
	v_exp_f32_e32 v87, v87
	v_exp_f32_e32 v88, v88
	v_exp_f32_e32 v89, v89
	v_add_f32_e32 v86, 1.0, v86
	v_add_f32_e32 v87, 1.0, v87
	v_add_f32_e32 v88, 1.0, v88
	v_add_f32_e32 v89, 1.0, v89
	v_rcp_f32_e32 v86, v86
	v_rcp_f32_e32 v87, v87
	v_rcp_f32_e32 v88, v88
	v_rcp_f32_e32 v89, v89
	v_mul_f32_e32 v86, v86, v82
	v_mul_f32_e32 v87, v87, v83
	v_mul_f32_e32 v88, v88, v84
	v_mul_f32_e32 v89, v89, v85
	v_mul_f32_e32 v86, v6, v86
	v_mul_f32_e32 v87, v7, v87
	v_mul_f32_e32 v88, v8, v88
	v_mul_f32_e32 v89, v9, v89
	v_cvt_pk_bf16_f32 v68, v86, v87
	v_cvt_pk_bf16_f32 v69, v88, v89
	global_store_dwordx2 v5, v[68:69], s[46:47]
	s_add_u32 s46, s46, 0x1000
	s_addc_u32 s47, s47, 0
	s_waitcnt vmcnt(9)
; __device__ __forceinline__ unsigned cvtpk(float lo, float hi) { unsigned r; asm volatile("v_cvt_pk_bf16_f32 %0, %1, %2" : "=v"(r) : "v"(lo), "v"(hi)); return r; }
; __device__ __forceinline__ float bflo(unsigned w) { return __uint_as_float(w << 16); }
; __device__ __forceinline__ float bfhi(unsigned w) { return __uint_as_float(w & 0xffff0000u); }
; __device__ __forceinline__ float gelu_tanh(float x) { const float u = 1.5957691216057308f * (x + 0.044715f * x * x * x); return x * sigmoidf_(u); }
; __global__ void __launch_bounds__(NTHREADS, 2) fwd_kernel(Args args) {
;     ...
;         for (int item = bx; item < NBATCH * NCH; item += G) {
;     ...
;             for (int t = 0; t < SCH; ++t) {
;                 const u32x4 pw = *(const u32x4*)(AB + (r0 + t) * D + 4 * tid);
;                 const f32x4 a = {__builtin_amdgcn_exp2f(bflo(pw.x)), __builtin_amdgcn_exp2f(bflo(pw.y)), __builtin_amdgcn_exp2f(bflo(pw.z)), __builtin_amdgcn_exp2f(bflo(pw.w))};
;                 const f32x4 bb = {bfhi(pw.x), bfhi(pw.y), bfhi(pw.z), bfhi(pw.w)};
;                 const u32x2 gw2 = *(const u32x2*)(U + (r0 + t) * (2 * D) + 4 * tid);
;                 h = a * h + bb;
;                 const float y0 = h.x * gelu_tanh(bflo(gw2.x)), y1 = h.y * gelu_tanh(bfhi(gw2.x)), y2 = h.z * gelu_tanh(bflo(gw2.y)), y3 = h.w * gelu_tanh(bfhi(gw2.y));
;                 u32x2 w; w.x = cvtpk(y0, y1); w.y = cvtpk(y2, y3);
;                 *(u32x2*)(Y + (r0 + t) * D + 4 * tid) = w;
;             }
	v_lshlrev_b32_e32 v78, 16, v46
	v_lshlrev_b32_e32 v79, 16, v47
	v_lshlrev_b32_e32 v80, 16, v48
	v_lshlrev_b32_e32 v81, 16, v49
	v_exp_f32_e32 v74, v78
	v_exp_f32_e32 v75, v79
	v_exp_f32_e32 v76, v80
	v_exp_f32_e32 v77, v81
	v_and_b32_e32 v46, 0xffff0000, v46
	v_and_b32_e32 v47, 0xffff0000, v47
	v_and_b32_e32 v48, 0xffff0000, v48
	v_and_b32_e32 v49, 0xffff0000, v49
	v_lshlrev_b32_e32 v82, 16, v50
	v_and_b32_e32 v83, 0xffff0000, v50
	v_lshlrev_b32_e32 v84, 16, v51
	v_and_b32_e32 v85, 0xffff0000, v51
	v_pk_fma_f32 v[6:7], v[6:7], v[74:75], v[46:47]
	v_pk_fma_f32 v[8:9], v[8:9], v[76:77], v[48:49]
	v_mul_f32_e32 v86, 0x3d372713, v82
	v_mul_f32_e32 v87, 0x3d372713, v83
	v_mul_f32_e32 v88, 0x3d372713, v84
	v_mul_f32_e32 v89, 0x3d372713, v85
	v_mul_f32_e32 v86, v86, v82
	v_mul_f32_e32 v87, v87, v83
	v_mul_f32_e32 v88, v88, v84
	v_mul_f32_e32 v89, v89, v85
	v_fma_f32 v86, v86, v82, v82
	v_fma_f32 v87, v87, v83, v83
	v_fma_f32 v88, v88, v84, v84
	v_fma_f32 v89, v89, v85, v85
	v_mul_f32_e32 v86, 0x3fcc422a, v86
	v_mul_f32_e32 v87, 0x3fcc422a, v87
	v_mul_f32_e32 v88, 0x3fcc422a, v88
	v_mul_f32_e32 v89, 0x3fcc422a, v89
	v_mul_f32_e32 v86, 0xbfb8aa3b, v86
	v_mul_f32_e32 v87, 0xbfb8aa3b, v87
	v_mul_f32_e32 v88, 0xbfb8aa3b, v88
	v_mul_f32_e32 v89, 0xbfb8aa3b, v89
	v_exp_f32_e32 v86, v86
	v_exp_f32_e32 v87, v87
	v_exp_f32_e32 v88, v88
	v_exp_f32_e32 v89, v89
	v_add_f32_e32 v86, 1.0, v86
	v_add_f32_e32 v87, 1.0, v87
	v_add_f32_e32 v88, 1.0, v88
	v_add_f32_e32 v89, 1.0, v89
	v_rcp_f32_e32 v86, v86
	v_rcp_f32_e32 v87, v87
	v_rcp_f32_e32 v88, v88
	v_rcp_f32_e32 v89, v89
	v_mul_f32_e32 v86, v86, v82
	v_mul_f32_e32 v87, v87, v83
	v_mul_f32_e32 v88, v88, v84
	v_mul_f32_e32 v89, v89, v85
	v_mul_f32_e32 v86, v6, v86
	v_mul_f32_e32 v87, v7, v87
	v_mul_f32_e32 v88, v8, v88
	v_mul_f32_e32 v89, v9, v89
	v_cvt_pk_bf16_f32 v70, v86, v87
	v_cvt_pk_bf16_f32 v71, v88, v89
	global_store_dwordx2 v5, v[70:71], s[46:47]
	s_add_u32 s46, s46, 0x1000
	s_addc_u32 s47, s47, 0
	s_waitcnt vmcnt(7)
	v_lshlrev_b32_e32 v78, 16, v52
	v_lshlrev_b32_e32 v79, 16, v53
	v_lshlrev_b32_e32 v80, 16, v54
	v_lshlrev_b32_e32 v81, 16, v55
	v_exp_f32_e32 v74, v78
	v_exp_f32_e32 v75, v79
	v_exp_f32_e32 v76, v80
	v_exp_f32_e32 v77, v81
	v_and_b32_e32 v52, 0xffff0000, v52
	v_and_b32_e32 v53, 0xffff0000, v53
	v_and_b32_e32 v54, 0xffff0000, v54
	v_and_b32_e32 v55, 0xffff0000, v55
	v_lshlrev_b32_e32 v82, 16, v56
	v_and_b32_e32 v83, 0xffff0000, v56
	v_lshlrev_b32_e32 v84, 16, v57
	v_and_b32_e32 v85, 0xffff0000, v57
	v_pk_fma_f32 v[6:7], v[6:7], v[74:75], v[52:53]
	v_pk_fma_f32 v[8:9], v[8:9], v[76:77], v[54:55]
	v_mul_f32_e32 v86, 0x3d372713, v82
	v_mul_f32_e32 v87, 0x3d372713, v83
	v_mul_f32_e32 v88, 0x3d372713, v84
	v_mul_f32_e32 v89, 0x3d372713, v85
	v_mul_f32_e32 v86, v86, v82
	v_mul_f32_e32 v87, v87, v83
	v_mul_f32_e32 v88, v88, v84
	v_mul_f32_e32 v89, v89, v85
	v_fma_f32 v86, v86, v82, v82
	v_fma_f32 v87, v87, v83, v83
	v_fma_f32 v88, v88, v84, v84
	v_fma_f32 v89, v89, v85, v85
	v_mul_f32_e32 v86, 0x3fcc422a, v86
	v_mul_f32_e32 v87, 0x3fcc422a, v87
	v_mul_f32_e32 v88, 0x3fcc422a, v88
	v_mul_f32_e32 v89, 0x3fcc422a, v89
	v_mul_f32_e32 v86, 0xbfb8aa3b, v86
	v_mul_f32_e32 v87, 0xbfb8aa3b, v87
	v_mul_f32_e32 v88, 0xbfb8aa3b, v88
	v_mul_f32_e32 v89, 0xbfb8aa3b, v89
	v_exp_f32_e32 v86, v86
	v_exp_f32_e32 v87, v87
	v_exp_f32_e32 v88, v88
	v_exp_f32_e32 v89, v89
	v_add_f32_e32 v86, 1.0, v86
	v_add_f32_e32 v87, 1.0, v87
	v_add_f32_e32 v88, 1.0, v88
	v_add_f32_e32 v89, 1.0, v89
	v_rcp_f32_e32 v86, v86
	v_rcp_f32_e32 v87, v87
	v_rcp_f32_e32 v88, v88
	v_rcp_f32_e32 v89, v89
	v_mul_f32_e32 v86, v86, v82
	v_mul_f32_e32 v87, v87, v83
	v_mul_f32_e32 v88, v88, v84
	v_mul_f32_e32 v89, v89, v85
	v_mul_f32_e32 v86, v6, v86
	v_mul_f32_e32 v87, v7, v87
	v_mul_f32_e32 v88, v8, v88
	v_mul_f32_e32 v89, v9, v89
	v_cvt_pk_bf16_f32 v72, v86, v87
	v_cvt_pk_bf16_f32 v73, v88, v89
	global_store_dwordx2 v5, v[72:73], s[46:47]
	s_add_u32 s46, s46, 0x1000
	s_addc_u32 s47, s47, 0
	s_add_u32 s62, s62, s76
	s_cmpk_gt_i32 s62, 0xff
	s_cbranch_scc0 .Lp5_item
